# strategy 7.5 (packed vs scalar fp32): packed f32 mul/fma/add in the four GEMM epilogues (SwiGLU, Bf16, Resid, QKV) split into scalar halves
# baseline (speedup 1.0000x reference)
.LBB0_630:
	s_mul_hi_i32 s13, s20, 0x78787879
	s_lshr_b32 s15, s13, 31
	s_ashr_i32 s13, s13, 3
	s_add_i32 s13, s13, s15
	s_lshl_b32 s2, s22, 2
	s_mul_i32 s13, s13, 17
	s_or_b32 s3, s2, s21
	s_sub_i32 s13, s20, s13
	s_add_i32 s2, s2, -12
	s_cmp_lt_u32 s2, 8
	s_cselect_b64 s[22:23], -1, 0
	s_cmp_lt_i32 s3, 8
	s_cselect_b64 s[24:25], -1, 0
	s_and_b64 s[26:27], s[24:25], exec
	s_cselect_b32 s2, 0, 64
	s_or_b64 vcc, s[24:25], s[22:23]
	s_and_b32 s15, s3, -2
	s_cmp_eq_u32 s15, 10
	s_cselect_b64 s[22:23], -1, 0
	s_cmp_gt_i32 s3, 27
	s_cselect_b64 s[24:25], -1, 0
	s_or_b64 s[22:23], s[24:25], s[22:23]
	s_cmp_lt_i32 s13, 16
	s_cselect_b64 s[24:25], -1, 0
	s_cmp_lt_i32 s3, 20
	s_movk_i32 s15, 0xc0
	s_cselect_b32 s15, 0x80, s15
	s_cmp_lt_i32 s3, 10
	s_cselect_b64 s[26:27], -1, 0
	s_and_b64 s[36:37], s[26:27], exec
	v_mbcnt_lo_u32_b32 v114, -1, 0
	v_mbcnt_hi_u32_b32 v114, -1, v114
	s_cselect_b32 s2, s2, s15
	v_and_b32_e32 v145, 15, v114
	v_ashrrev_i32_e32 v114, 4, v114
	s_and_b64 s[24:25], s[26:27], s[24:25]
	s_lshl_b32 s2, s2, 2
	v_lshlrev_b32_e32 v138, 3, v114
	s_add_u32 s26, s8, s2
	s_addc_u32 s27, s9, 0
	v_ashrrev_i32_e32 v139, 31, v138
	s_lshl_b32 s2, s13, 2
	v_cmp_gt_u32_e64 s[36:37], 2, v114
	v_cndmask_b32_e64 v114, 0, 1, s[24:25]
	v_cndmask_b32_e32 v146, 1.0, v236, vcc
	v_lshl_add_u64 v[136:137], v[138:139], 2, s[26:27]
	s_add_i32 s2, s2, s46
	v_and_b32_e32 v139, 8, v138
	s_and_b64 vcc, exec, s[22:23]
	v_cmp_ne_u32_e64 s[38:39], 1, v114
	s_lshl_b32 s13, s20, 8
	s_add_i32 s13, s13, s29
	v_or_b32_e32 v114, s13, v145
	v_lshl_add_u32 v147, s3, 6, v138
	v_mul_u32_u24_e32 v114, 0x1200, v114
	v_lshl_add_u32 v114, v147, 1, v114
	s_mov_b32 s26, s4
	s_mov_b32 s27, s5
	s_and_b64 vcc, exec, s[22:23]
	s_cbranch_vccnz .Lqkv_epi_v
	global_load_dwordx4 v[148:151], v[136:137], off
	global_load_dwordx4 v[152:155], v[136:137], off offset:16
	global_load_dwordx4 v[156:159], v[136:137], off offset:128
	global_load_dwordx4 v[160:163], v[136:137], off offset:144
	s_and_b64 vcc, exec, s[24:25]
	s_cbranch_vccz .Lqkv_epi_norope
	v_lshlrev_b32_e32 v147, 2, v139
	v_lshl_add_u32 v136, v145, 6, v147
	v_mov_b32_e32 v138, v147
	v_add_u32_e32 v139, 0x1000, v147
	v_add_u32_e32 v137, 0x1000, v136
	s_lshl_b32 s15, s2, 6
	s_add_u32 s40, s6, s15
	s_addc_u32 s41, s7, 0
	global_load_dwordx4 v[164:167], v138, s[40:41]
	global_load_dwordx4 v[168:171], v138, s[40:41] offset:16
	global_load_dwordx4 v[172:175], v139, s[40:41]
	global_load_dwordx4 v[176:179], v139, s[40:41] offset:16
	global_load_dwordx4 v[180:183], v136, s[6:7]
	global_load_dwordx4 v[184:187], v136, s[6:7] offset:16
	global_load_dwordx4 v[202:205], v137, s[6:7]
	global_load_dwordx4 v[206:209], v137, s[6:7] offset:16
	global_load_dwordx4 v[210:213], v136, s[6:7] offset:1024
	global_load_dwordx4 v[214:217], v136, s[6:7] offset:1040
	global_load_dwordx4 v[218:221], v137, s[6:7] offset:1024
	global_load_dwordx4 v[222:225], v137, s[6:7] offset:1040
	v_mul_f32_e32 v132, v116, v116
	v_mul_f32_e32 v133, v117, v117
	v_mul_f32_e32 v134, v124, v124
	v_mul_f32_e32 v135, v125, v125
	v_fma_f32 v132, v118, v118, v132
	v_fma_f32 v133, v119, v119, v133
	v_fma_f32 v134, v126, v126, v134
	v_fma_f32 v135, v127, v127, v135
	v_fma_f32 v132, v120, v120, v132
	v_fma_f32 v133, v121, v121, v133
	v_fma_f32 v134, v128, v128, v134
	v_fma_f32 v135, v129, v129, v135
	v_fma_f32 v132, v122, v122, v132
	v_fma_f32 v133, v123, v123, v133
	v_fma_f32 v134, v130, v130, v134
	v_fma_f32 v135, v131, v131, v135
	v_add_f32_e32 v132, v132, v134
	v_add_f32_e32 v133, v133, v135
	s_nop 0
	v_add_f32_e32 v194, v132, v133
	ds_swizzle_b32 v195, v194 offset:swizzle(SWAP,16)
	s_waitcnt lgkmcnt(0)
	v_add_f32_e32 v194, v194, v195
	v_mov_b32_e32 v195, v194
	s_nop 1
	v_permlane32_swap_b32_e32 v194, v195
	v_add_f32_e32 v194, v194, v195
	v_fmamk_f32 v194, v194, 0x3c800000, v192
	v_rsq_f32_e32 v194, v194
	s_nop 0
	v_mul_f32_e32 v196, v146, v194
	v_mul_f32_e32 v116, v116, v196
	v_mul_f32_e32 v117, v117, v196
	v_mul_f32_e32 v118, v118, v196
	v_mul_f32_e32 v119, v119, v196
	v_mul_f32_e32 v120, v120, v196
	v_mul_f32_e32 v121, v121, v196
	v_mul_f32_e32 v122, v122, v196
	v_mul_f32_e32 v123, v123, v196
	v_mul_f32_e32 v124, v124, v196
	v_mul_f32_e32 v125, v125, v196
	v_mul_f32_e32 v126, v126, v196
	v_mul_f32_e32 v127, v127, v196
	v_mul_f32_e32 v128, v128, v196
	v_mul_f32_e32 v129, v129, v196
	v_mul_f32_e32 v130, v130, v196
	v_mul_f32_e32 v131, v131, v196
	s_waitcnt vmcnt(12)
	v_mul_f32_e32 v116, v148, v116
	v_mul_f32_e32 v117, v149, v117
	v_mul_f32_e32 v118, v150, v118
	v_mul_f32_e32 v119, v151, v119
	v_mul_f32_e32 v120, v152, v120
	v_mul_f32_e32 v121, v153, v121
	v_mul_f32_e32 v122, v154, v122
	v_mul_f32_e32 v123, v155, v123
	v_mul_f32_e32 v124, v156, v124
	v_mul_f32_e32 v125, v157, v125
	v_mul_f32_e32 v126, v158, v126
	v_mul_f32_e32 v127, v159, v127
	v_mul_f32_e32 v128, v160, v128
	v_mul_f32_e32 v129, v161, v129
	v_mul_f32_e32 v130, v162, v130
	v_mul_f32_e32 v131, v163, v131
	s_waitcnt vmcnt(8)
	v_mul_f32_e32 v226, v116, v172
	v_mul_f32_e32 v227, v117, v173
	v_mul_f32_e32 v228, v118, v174
	v_mul_f32_e32 v229, v119, v175
	v_mul_f32_e32 v230, v120, v176
	v_mul_f32_e32 v231, v121, v177
	v_mul_f32_e32 v232, v122, v178
	v_mul_f32_e32 v233, v123, v179
	v_mov_b64_e32 v[244:245], v[226:227]
	v_mov_b64_e32 v[246:247], v[228:229]
	v_mov_b64_e32 v[248:249], v[230:231]
	v_mov_b64_e32 v[250:251], v[232:233]
	v_permlane32_swap_b32_e32 v226, v244
	v_permlane32_swap_b32_e32 v227, v245
	v_permlane32_swap_b32_e32 v228, v246
	v_permlane32_swap_b32_e32 v229, v247
	v_permlane32_swap_b32_e32 v230, v248
	v_permlane32_swap_b32_e32 v231, v249
	v_permlane32_swap_b32_e32 v232, v250
	v_permlane32_swap_b32_e32 v233, v251
	v_cndmask_b32_e64 v244, v226, -v244, s[36:37]
	v_cndmask_b32_e64 v245, v227, -v245, s[36:37]
	v_cndmask_b32_e64 v246, v228, -v246, s[36:37]
	v_cndmask_b32_e64 v247, v229, -v247, s[36:37]
	v_cndmask_b32_e64 v248, v230, -v248, s[36:37]
	v_cndmask_b32_e64 v249, v231, -v249, s[36:37]
	v_cndmask_b32_e64 v250, v232, -v250, s[36:37]
	v_cndmask_b32_e64 v251, v233, -v251, s[36:37]
	v_fma_f32 v116, v116, v164, v244
	v_fma_f32 v117, v117, v165, v245
	v_fma_f32 v118, v118, v166, v246
	v_fma_f32 v119, v119, v167, v247
	v_fma_f32 v120, v120, v168, v248
	v_fma_f32 v121, v121, v169, v249
	v_fma_f32 v122, v122, v170, v250
	v_fma_f32 v123, v123, v171, v251
	s_waitcnt vmcnt(4)
	v_mul_f32_e32 v226, v124, v202
	v_mul_f32_e32 v227, v125, v203
	v_mul_f32_e32 v228, v126, v204
	v_mul_f32_e32 v229, v127, v205
	v_mul_f32_e32 v230, v128, v206
	v_mul_f32_e32 v231, v129, v207
	v_mul_f32_e32 v232, v130, v208
	v_mul_f32_e32 v233, v131, v209
	v_mov_b64_e32 v[244:245], v[226:227]
	v_mov_b64_e32 v[246:247], v[228:229]
	v_mov_b64_e32 v[248:249], v[230:231]
	v_mov_b64_e32 v[250:251], v[232:233]
	v_permlane32_swap_b32_e32 v226, v244
	v_permlane32_swap_b32_e32 v227, v245
	v_permlane32_swap_b32_e32 v228, v246
	v_permlane32_swap_b32_e32 v229, v247
	v_permlane32_swap_b32_e32 v230, v248
	v_permlane32_swap_b32_e32 v231, v249
	v_permlane32_swap_b32_e32 v232, v250
	v_permlane32_swap_b32_e32 v233, v251
	v_cndmask_b32_e64 v244, v226, -v244, s[36:37]
	v_cndmask_b32_e64 v245, v227, -v245, s[36:37]
	v_cndmask_b32_e64 v246, v228, -v246, s[36:37]
	v_cndmask_b32_e64 v247, v229, -v247, s[36:37]
	v_cndmask_b32_e64 v248, v230, -v248, s[36:37]
	v_cndmask_b32_e64 v249, v231, -v249, s[36:37]
	v_cndmask_b32_e64 v250, v232, -v250, s[36:37]
	v_cndmask_b32_e64 v251, v233, -v251, s[36:37]
	v_fma_f32 v124, v124, v180, v244
	v_fma_f32 v125, v125, v181, v245
	v_fma_f32 v126, v126, v182, v246
	v_fma_f32 v127, v127, v183, v247
	v_fma_f32 v128, v128, v184, v248
	v_fma_f32 v129, v129, v185, v249
	v_fma_f32 v130, v130, v186, v250
	v_fma_f32 v131, v131, v187, v251
	global_load_dwordx4 v[180:183], v136, s[6:7] offset:2048
	global_load_dwordx4 v[184:187], v136, s[6:7] offset:2064
	global_load_dwordx4 v[202:205], v137, s[6:7] offset:2048
	global_load_dwordx4 v[206:209], v137, s[6:7] offset:2064
	v_cvt_pk_bf16_f32 v116, v116, v117
	v_cvt_pk_bf16_f32 v117, v118, v119
	v_cvt_pk_bf16_f32 v118, v120, v121
	v_cvt_pk_bf16_f32 v119, v122, v123
	global_store_dwordx4 v114, v[116:119], s[26:27]
	v_cvt_pk_bf16_f32 v124, v124, v125
	v_cvt_pk_bf16_f32 v125, v126, v127
	v_cvt_pk_bf16_f32 v126, v128, v129
	v_cvt_pk_bf16_f32 v127, v130, v131
	global_store_dwordx4 v114, v[124:127], s[26:27] offset:64
	s_add_u32 s26, s26, 0x12000
	s_addc_u32 s27, s27, 0
	v_mul_f32_e32 v132, v98, v98
	v_mul_f32_e32 v133, v99, v99
	v_mul_f32_e32 v134, v106, v106
	v_mul_f32_e32 v135, v107, v107
	v_fma_f32 v132, v100, v100, v132
	v_fma_f32 v133, v101, v101, v133
	v_fma_f32 v134, v108, v108, v134
	v_fma_f32 v135, v109, v109, v135
	v_fma_f32 v132, v102, v102, v132
	v_fma_f32 v133, v103, v103, v133
	v_fma_f32 v134, v110, v110, v134
	v_fma_f32 v135, v111, v111, v135
	v_fma_f32 v132, v104, v104, v132
	v_fma_f32 v133, v105, v105, v133
	v_fma_f32 v134, v112, v112, v134
	v_fma_f32 v135, v113, v113, v135
	v_add_f32_e32 v132, v132, v134
	v_add_f32_e32 v133, v133, v135
	s_nop 0
	v_add_f32_e32 v194, v132, v133
	ds_swizzle_b32 v195, v194 offset:swizzle(SWAP,16)
	s_waitcnt lgkmcnt(0)
	v_add_f32_e32 v194, v194, v195
	v_mov_b32_e32 v195, v194
	s_nop 1
	v_permlane32_swap_b32_e32 v194, v195
	v_add_f32_e32 v194, v194, v195
	v_fmamk_f32 v194, v194, 0x3c800000, v192
	v_rsq_f32_e32 v194, v194
	s_nop 0
	v_mul_f32_e32 v196, v146, v194
	v_mul_f32_e32 v98, v98, v196
	v_mul_f32_e32 v99, v99, v196
	v_mul_f32_e32 v100, v100, v196
	v_mul_f32_e32 v101, v101, v196
	v_mul_f32_e32 v102, v102, v196
	v_mul_f32_e32 v103, v103, v196
	v_mul_f32_e32 v104, v104, v196
	v_mul_f32_e32 v105, v105, v196
	v_mul_f32_e32 v106, v106, v196
	v_mul_f32_e32 v107, v107, v196
	v_mul_f32_e32 v108, v108, v196
	v_mul_f32_e32 v109, v109, v196
	v_mul_f32_e32 v110, v110, v196
	v_mul_f32_e32 v111, v111, v196
	v_mul_f32_e32 v112, v112, v196
	v_mul_f32_e32 v113, v113, v196
	v_mul_f32_e32 v98, v148, v98
	v_mul_f32_e32 v99, v149, v99
	v_mul_f32_e32 v100, v150, v100
	v_mul_f32_e32 v101, v151, v101
	v_mul_f32_e32 v102, v152, v102
	v_mul_f32_e32 v103, v153, v103
	v_mul_f32_e32 v104, v154, v104
	v_mul_f32_e32 v105, v155, v105
	v_mul_f32_e32 v106, v156, v106
	v_mul_f32_e32 v107, v157, v107
	v_mul_f32_e32 v108, v158, v108
	v_mul_f32_e32 v109, v159, v109
	v_mul_f32_e32 v110, v160, v110
	v_mul_f32_e32 v111, v161, v111
	v_mul_f32_e32 v112, v162, v112
	v_mul_f32_e32 v113, v163, v113
	v_mul_f32_e32 v226, v98, v172
	v_mul_f32_e32 v227, v99, v173
	v_mul_f32_e32 v228, v100, v174
	v_mul_f32_e32 v229, v101, v175
	v_mul_f32_e32 v230, v102, v176
	v_mul_f32_e32 v231, v103, v177
	v_mul_f32_e32 v232, v104, v178
	v_mul_f32_e32 v233, v105, v179
	v_mov_b64_e32 v[244:245], v[226:227]
	v_mov_b64_e32 v[246:247], v[228:229]
	v_mov_b64_e32 v[248:249], v[230:231]
	v_mov_b64_e32 v[250:251], v[232:233]
	v_permlane32_swap_b32_e32 v226, v244
	v_permlane32_swap_b32_e32 v227, v245
	v_permlane32_swap_b32_e32 v228, v246
	v_permlane32_swap_b32_e32 v229, v247
	v_permlane32_swap_b32_e32 v230, v248
	v_permlane32_swap_b32_e32 v231, v249
	v_permlane32_swap_b32_e32 v232, v250
	v_permlane32_swap_b32_e32 v233, v251
	v_cndmask_b32_e64 v244, v226, -v244, s[36:37]
	v_cndmask_b32_e64 v245, v227, -v245, s[36:37]
	v_cndmask_b32_e64 v246, v228, -v246, s[36:37]
	v_cndmask_b32_e64 v247, v229, -v247, s[36:37]
	v_cndmask_b32_e64 v248, v230, -v248, s[36:37]
	v_cndmask_b32_e64 v249, v231, -v249, s[36:37]
	v_cndmask_b32_e64 v250, v232, -v250, s[36:37]
	v_cndmask_b32_e64 v251, v233, -v251, s[36:37]
	v_fma_f32 v98, v98, v164, v244
	v_fma_f32 v99, v99, v165, v245
	v_fma_f32 v100, v100, v166, v246
	v_fma_f32 v101, v101, v167, v247
	v_fma_f32 v102, v102, v168, v248
	v_fma_f32 v103, v103, v169, v249
	v_fma_f32 v104, v104, v170, v250
	v_fma_f32 v105, v105, v171, v251
	s_waitcnt vmcnt(6)
	v_mul_f32_e32 v226, v106, v218
	v_mul_f32_e32 v227, v107, v219
	v_mul_f32_e32 v228, v108, v220
	v_mul_f32_e32 v229, v109, v221
	v_mul_f32_e32 v230, v110, v222
	v_mul_f32_e32 v231, v111, v223
	v_mul_f32_e32 v232, v112, v224
	v_mul_f32_e32 v233, v113, v225
	v_mov_b64_e32 v[244:245], v[226:227]
	v_mov_b64_e32 v[246:247], v[228:229]
	v_mov_b64_e32 v[248:249], v[230:231]
	v_mov_b64_e32 v[250:251], v[232:233]
	v_permlane32_swap_b32_e32 v226, v244
	v_permlane32_swap_b32_e32 v227, v245
	v_permlane32_swap_b32_e32 v228, v246
	v_permlane32_swap_b32_e32 v229, v247
	v_permlane32_swap_b32_e32 v230, v248
	v_permlane32_swap_b32_e32 v231, v249
	v_permlane32_swap_b32_e32 v232, v250
	v_permlane32_swap_b32_e32 v233, v251
	v_cndmask_b32_e64 v244, v226, -v244, s[36:37]
	v_cndmask_b32_e64 v245, v227, -v245, s[36:37]
	v_cndmask_b32_e64 v246, v228, -v246, s[36:37]
	v_cndmask_b32_e64 v247, v229, -v247, s[36:37]
	v_cndmask_b32_e64 v248, v230, -v248, s[36:37]
	v_cndmask_b32_e64 v249, v231, -v249, s[36:37]
	v_cndmask_b32_e64 v250, v232, -v250, s[36:37]
	v_cndmask_b32_e64 v251, v233, -v251, s[36:37]
	v_fma_f32 v106, v106, v210, v244
	v_fma_f32 v107, v107, v211, v245
	v_fma_f32 v108, v108, v212, v246
	v_fma_f32 v109, v109, v213, v247
	v_fma_f32 v110, v110, v214, v248
	v_fma_f32 v111, v111, v215, v249
	v_fma_f32 v112, v112, v216, v250
	v_fma_f32 v113, v113, v217, v251
	global_load_dwordx4 v[210:213], v136, s[6:7] offset:3072
	global_load_dwordx4 v[214:217], v136, s[6:7] offset:3088
	global_load_dwordx4 v[218:221], v137, s[6:7] offset:3072
	global_load_dwordx4 v[222:225], v137, s[6:7] offset:3088
	v_cvt_pk_bf16_f32 v98, v98, v99
	v_cvt_pk_bf16_f32 v99, v100, v101
	v_cvt_pk_bf16_f32 v100, v102, v103
	v_cvt_pk_bf16_f32 v101, v104, v105
	global_store_dwordx4 v114, v[98:101], s[26:27]
	v_cvt_pk_bf16_f32 v106, v106, v107
	v_cvt_pk_bf16_f32 v107, v108, v109
	v_cvt_pk_bf16_f32 v108, v110, v111
	v_cvt_pk_bf16_f32 v109, v112, v113
	global_store_dwordx4 v114, v[106:109], s[26:27] offset:64
	s_add_u32 s26, s26, 0x12000
	s_addc_u32 s27, s27, 0
	v_mul_f32_e32 v132, v82, v82
	v_mul_f32_e32 v133, v83, v83
	v_mul_f32_e32 v134, v90, v90
	v_mul_f32_e32 v135, v91, v91
	v_fma_f32 v132, v84, v84, v132
	v_fma_f32 v133, v85, v85, v133
	v_fma_f32 v134, v92, v92, v134
	v_fma_f32 v135, v93, v93, v135
	v_fma_f32 v132, v86, v86, v132
	v_fma_f32 v133, v87, v87, v133
	v_fma_f32 v134, v94, v94, v134
	v_fma_f32 v135, v95, v95, v135
	v_fma_f32 v132, v88, v88, v132
	v_fma_f32 v133, v89, v89, v133
	v_fma_f32 v134, v96, v96, v134
	v_fma_f32 v135, v97, v97, v135
	v_add_f32_e32 v132, v132, v134
	v_add_f32_e32 v133, v133, v135
	s_nop 0
	v_add_f32_e32 v194, v132, v133
	ds_swizzle_b32 v195, v194 offset:swizzle(SWAP,16)
	s_waitcnt lgkmcnt(0)
	v_add_f32_e32 v194, v194, v195
	v_mov_b32_e32 v195, v194
	s_nop 1
	v_permlane32_swap_b32_e32 v194, v195
	v_add_f32_e32 v194, v194, v195
	v_fmamk_f32 v194, v194, 0x3c800000, v192
	v_rsq_f32_e32 v194, v194
	s_nop 0
	v_mul_f32_e32 v196, v146, v194
	v_mul_f32_e32 v82, v82, v196
	v_mul_f32_e32 v83, v83, v196
	v_mul_f32_e32 v84, v84, v196
	v_mul_f32_e32 v85, v85, v196
	v_mul_f32_e32 v86, v86, v196
	v_mul_f32_e32 v87, v87, v196
	v_mul_f32_e32 v88, v88, v196
	v_mul_f32_e32 v89, v89, v196
	v_mul_f32_e32 v90, v90, v196
	v_mul_f32_e32 v91, v91, v196
	v_mul_f32_e32 v92, v92, v196
	v_mul_f32_e32 v93, v93, v196
	v_mul_f32_e32 v94, v94, v196
	v_mul_f32_e32 v95, v95, v196
	v_mul_f32_e32 v96, v96, v196
	v_mul_f32_e32 v97, v97, v196
	v_mul_f32_e32 v82, v148, v82
	v_mul_f32_e32 v83, v149, v83
	v_mul_f32_e32 v84, v150, v84
	v_mul_f32_e32 v85, v151, v85
	v_mul_f32_e32 v86, v152, v86
	v_mul_f32_e32 v87, v153, v87
	v_mul_f32_e32 v88, v154, v88
	v_mul_f32_e32 v89, v155, v89
	v_mul_f32_e32 v90, v156, v90
	v_mul_f32_e32 v91, v157, v91
	v_mul_f32_e32 v92, v158, v92
	v_mul_f32_e32 v93, v159, v93
	v_mul_f32_e32 v94, v160, v94
	v_mul_f32_e32 v95, v161, v95
	v_mul_f32_e32 v96, v162, v96
	v_mul_f32_e32 v97, v163, v97
	v_mul_f32_e32 v226, v82, v172
	v_mul_f32_e32 v227, v83, v173
	v_mul_f32_e32 v228, v84, v174
	v_mul_f32_e32 v229, v85, v175
	v_mul_f32_e32 v230, v86, v176
	v_mul_f32_e32 v231, v87, v177
	v_mul_f32_e32 v232, v88, v178
	v_mul_f32_e32 v233, v89, v179
	v_mov_b64_e32 v[244:245], v[226:227]
	v_mov_b64_e32 v[246:247], v[228:229]
	v_mov_b64_e32 v[248:249], v[230:231]
	v_mov_b64_e32 v[250:251], v[232:233]
	v_permlane32_swap_b32_e32 v226, v244
	v_permlane32_swap_b32_e32 v227, v245
	v_permlane32_swap_b32_e32 v228, v246
	v_permlane32_swap_b32_e32 v229, v247
	v_permlane32_swap_b32_e32 v230, v248
	v_permlane32_swap_b32_e32 v231, v249
	v_permlane32_swap_b32_e32 v232, v250
	v_permlane32_swap_b32_e32 v233, v251
	v_cndmask_b32_e64 v244, v226, -v244, s[36:37]
	v_cndmask_b32_e64 v245, v227, -v245, s[36:37]
	v_cndmask_b32_e64 v246, v228, -v246, s[36:37]
	v_cndmask_b32_e64 v247, v229, -v247, s[36:37]
	v_cndmask_b32_e64 v248, v230, -v248, s[36:37]
	v_cndmask_b32_e64 v249, v231, -v249, s[36:37]
	v_cndmask_b32_e64 v250, v232, -v250, s[36:37]
	v_cndmask_b32_e64 v251, v233, -v251, s[36:37]
	v_fma_f32 v82, v82, v164, v244
	v_fma_f32 v83, v83, v165, v245
	v_fma_f32 v84, v84, v166, v246
	v_fma_f32 v85, v85, v167, v247
	v_fma_f32 v86, v86, v168, v248
	v_fma_f32 v87, v87, v169, v249
	v_fma_f32 v88, v88, v170, v250
	v_fma_f32 v89, v89, v171, v251
	s_waitcnt vmcnt(8)
	v_mul_f32_e32 v226, v90, v202
	v_mul_f32_e32 v227, v91, v203
	v_mul_f32_e32 v228, v92, v204
	v_mul_f32_e32 v229, v93, v205
	v_mul_f32_e32 v230, v94, v206
	v_mul_f32_e32 v231, v95, v207
	v_mul_f32_e32 v232, v96, v208
	v_mul_f32_e32 v233, v97, v209
	v_mov_b64_e32 v[244:245], v[226:227]
	v_mov_b64_e32 v[246:247], v[228:229]
	v_mov_b64_e32 v[248:249], v[230:231]
	v_mov_b64_e32 v[250:251], v[232:233]
	v_permlane32_swap_b32_e32 v226, v244
	v_permlane32_swap_b32_e32 v227, v245
	v_permlane32_swap_b32_e32 v228, v246
	v_permlane32_swap_b32_e32 v229, v247
	v_permlane32_swap_b32_e32 v230, v248
	v_permlane32_swap_b32_e32 v231, v249
	v_permlane32_swap_b32_e32 v232, v250
	v_permlane32_swap_b32_e32 v233, v251
	v_cndmask_b32_e64 v244, v226, -v244, s[36:37]
	v_cndmask_b32_e64 v245, v227, -v245, s[36:37]
	v_cndmask_b32_e64 v246, v228, -v246, s[36:37]
	v_cndmask_b32_e64 v247, v229, -v247, s[36:37]
	v_cndmask_b32_e64 v248, v230, -v248, s[36:37]
	v_cndmask_b32_e64 v249, v231, -v249, s[36:37]
	v_cndmask_b32_e64 v250, v232, -v250, s[36:37]
	v_cndmask_b32_e64 v251, v233, -v251, s[36:37]
	v_fma_f32 v90, v90, v180, v244
	v_fma_f32 v91, v91, v181, v245
	v_fma_f32 v92, v92, v182, v246
	v_fma_f32 v93, v93, v183, v247
	v_fma_f32 v94, v94, v184, v248
	v_fma_f32 v95, v95, v185, v249
	v_fma_f32 v96, v96, v186, v250
	v_fma_f32 v97, v97, v187, v251
	global_load_dwordx4 v[180:183], v136, s[6:7]
	global_load_dwordx4 v[184:187], v136, s[6:7] offset:16
	global_load_dwordx4 v[202:205], v137, s[6:7]
	global_load_dwordx4 v[206:209], v137, s[6:7] offset:16
	v_cvt_pk_bf16_f32 v82, v82, v83
	v_cvt_pk_bf16_f32 v83, v84, v85
	v_cvt_pk_bf16_f32 v84, v86, v87
	v_cvt_pk_bf16_f32 v85, v88, v89
	global_store_dwordx4 v114, v[82:85], s[26:27]
	v_cvt_pk_bf16_f32 v90, v90, v91
	v_cvt_pk_bf16_f32 v91, v92, v93
	v_cvt_pk_bf16_f32 v92, v94, v95
	v_cvt_pk_bf16_f32 v93, v96, v97
	global_store_dwordx4 v114, v[90:93], s[26:27] offset:64
	s_add_u32 s26, s26, 0x12000
	s_addc_u32 s27, s27, 0
	v_mul_f32_e32 v132, v66, v66
	v_mul_f32_e32 v133, v67, v67
	v_mul_f32_e32 v134, v74, v74
	v_mul_f32_e32 v135, v75, v75
	v_fma_f32 v132, v68, v68, v132
	v_fma_f32 v133, v69, v69, v133
	v_fma_f32 v134, v76, v76, v134
	v_fma_f32 v135, v77, v77, v135
	v_fma_f32 v132, v70, v70, v132
	v_fma_f32 v133, v71, v71, v133
	v_fma_f32 v134, v78, v78, v134
	v_fma_f32 v135, v79, v79, v135
	v_fma_f32 v132, v72, v72, v132
	v_fma_f32 v133, v73, v73, v133
	v_fma_f32 v134, v80, v80, v134
	v_fma_f32 v135, v81, v81, v135
	v_add_f32_e32 v132, v132, v134
	v_add_f32_e32 v133, v133, v135
	s_nop 0
	v_add_f32_e32 v194, v132, v133
	ds_swizzle_b32 v195, v194 offset:swizzle(SWAP,16)
	s_waitcnt lgkmcnt(0)
	v_add_f32_e32 v194, v194, v195
	v_mov_b32_e32 v195, v194
	s_nop 1
	v_permlane32_swap_b32_e32 v194, v195
	v_add_f32_e32 v194, v194, v195
	v_fmamk_f32 v194, v194, 0x3c800000, v192
	v_rsq_f32_e32 v194, v194
	s_nop 0
	v_mul_f32_e32 v196, v146, v194
	v_mul_f32_e32 v66, v66, v196
	v_mul_f32_e32 v67, v67, v196
	v_mul_f32_e32 v68, v68, v196
	v_mul_f32_e32 v69, v69, v196
	v_mul_f32_e32 v70, v70, v196
	v_mul_f32_e32 v71, v71, v196
	v_mul_f32_e32 v72, v72, v196
	v_mul_f32_e32 v73, v73, v196
	v_mul_f32_e32 v74, v74, v196
	v_mul_f32_e32 v75, v75, v196
	v_mul_f32_e32 v76, v76, v196
	v_mul_f32_e32 v77, v77, v196
	v_mul_f32_e32 v78, v78, v196
	v_mul_f32_e32 v79, v79, v196
	v_mul_f32_e32 v80, v80, v196
	v_mul_f32_e32 v81, v81, v196
	v_mul_f32_e32 v66, v148, v66
	v_mul_f32_e32 v67, v149, v67
	v_mul_f32_e32 v68, v150, v68
	v_mul_f32_e32 v69, v151, v69
	v_mul_f32_e32 v70, v152, v70
	v_mul_f32_e32 v71, v153, v71
	v_mul_f32_e32 v72, v154, v72
	v_mul_f32_e32 v73, v155, v73
	v_mul_f32_e32 v74, v156, v74
	v_mul_f32_e32 v75, v157, v75
	v_mul_f32_e32 v76, v158, v76
	v_mul_f32_e32 v77, v159, v77
	v_mul_f32_e32 v78, v160, v78
	v_mul_f32_e32 v79, v161, v79
	v_mul_f32_e32 v80, v162, v80
	v_mul_f32_e32 v81, v163, v81
	v_mul_f32_e32 v226, v66, v172
	v_mul_f32_e32 v227, v67, v173
	v_mul_f32_e32 v228, v68, v174
	v_mul_f32_e32 v229, v69, v175
	v_mul_f32_e32 v230, v70, v176
	v_mul_f32_e32 v231, v71, v177
	v_mul_f32_e32 v232, v72, v178
	v_mul_f32_e32 v233, v73, v179
	v_mov_b64_e32 v[244:245], v[226:227]
	v_mov_b64_e32 v[246:247], v[228:229]
	v_mov_b64_e32 v[248:249], v[230:231]
	v_mov_b64_e32 v[250:251], v[232:233]
	v_permlane32_swap_b32_e32 v226, v244
	v_permlane32_swap_b32_e32 v227, v245
	v_permlane32_swap_b32_e32 v228, v246
	v_permlane32_swap_b32_e32 v229, v247
	v_permlane32_swap_b32_e32 v230, v248
	v_permlane32_swap_b32_e32 v231, v249
	v_permlane32_swap_b32_e32 v232, v250
	v_permlane32_swap_b32_e32 v233, v251
	v_cndmask_b32_e64 v244, v226, -v244, s[36:37]
	v_cndmask_b32_e64 v245, v227, -v245, s[36:37]
	v_cndmask_b32_e64 v246, v228, -v246, s[36:37]
	v_cndmask_b32_e64 v247, v229, -v247, s[36:37]
	v_cndmask_b32_e64 v248, v230, -v248, s[36:37]
	v_cndmask_b32_e64 v249, v231, -v249, s[36:37]
	v_cndmask_b32_e64 v250, v232, -v250, s[36:37]
	v_cndmask_b32_e64 v251, v233, -v251, s[36:37]
	v_fma_f32 v66, v66, v164, v244
	v_fma_f32 v67, v67, v165, v245
	v_fma_f32 v68, v68, v166, v246
	v_fma_f32 v69, v69, v167, v247
	v_fma_f32 v70, v70, v168, v248
	v_fma_f32 v71, v71, v169, v249
	v_fma_f32 v72, v72, v170, v250
	v_fma_f32 v73, v73, v171, v251
	s_add_u32 s40, s40, 0x80
	s_addc_u32 s41, s41, 0
	global_load_dwordx4 v[164:167], v138, s[40:41]
	global_load_dwordx4 v[168:171], v138, s[40:41] offset:16
	global_load_dwordx4 v[172:175], v139, s[40:41]
	global_load_dwordx4 v[176:179], v139, s[40:41] offset:16
	s_waitcnt vmcnt(12)
	v_mul_f32_e32 v226, v74, v218
	v_mul_f32_e32 v227, v75, v219
	v_mul_f32_e32 v228, v76, v220
	v_mul_f32_e32 v229, v77, v221
	v_mul_f32_e32 v230, v78, v222
	v_mul_f32_e32 v231, v79, v223
	v_mul_f32_e32 v232, v80, v224
	v_mul_f32_e32 v233, v81, v225
	v_mov_b64_e32 v[244:245], v[226:227]
	v_mov_b64_e32 v[246:247], v[228:229]
	v_mov_b64_e32 v[248:249], v[230:231]
	v_mov_b64_e32 v[250:251], v[232:233]
	v_permlane32_swap_b32_e32 v226, v244
	v_permlane32_swap_b32_e32 v227, v245
	v_permlane32_swap_b32_e32 v228, v246
	v_permlane32_swap_b32_e32 v229, v247
	v_permlane32_swap_b32_e32 v230, v248
	v_permlane32_swap_b32_e32 v231, v249
	v_permlane32_swap_b32_e32 v232, v250
	v_permlane32_swap_b32_e32 v233, v251
	v_cndmask_b32_e64 v244, v226, -v244, s[36:37]
	v_cndmask_b32_e64 v245, v227, -v245, s[36:37]
	v_cndmask_b32_e64 v246, v228, -v246, s[36:37]
	v_cndmask_b32_e64 v247, v229, -v247, s[36:37]
	v_cndmask_b32_e64 v248, v230, -v248, s[36:37]
	v_cndmask_b32_e64 v249, v231, -v249, s[36:37]
	v_cndmask_b32_e64 v250, v232, -v250, s[36:37]
	v_cndmask_b32_e64 v251, v233, -v251, s[36:37]
	v_fma_f32 v74, v74, v210, v244
	v_fma_f32 v75, v75, v211, v245
	v_fma_f32 v76, v76, v212, v246
	v_fma_f32 v77, v77, v213, v247
	v_fma_f32 v78, v78, v214, v248
	v_fma_f32 v79, v79, v215, v249
	v_fma_f32 v80, v80, v216, v250
	v_fma_f32 v81, v81, v217, v251
	global_load_dwordx4 v[210:213], v136, s[6:7] offset:1024
	global_load_dwordx4 v[214:217], v136, s[6:7] offset:1040
	global_load_dwordx4 v[218:221], v137, s[6:7] offset:1024
	global_load_dwordx4 v[222:225], v137, s[6:7] offset:1040
	v_cvt_pk_bf16_f32 v66, v66, v67
	v_cvt_pk_bf16_f32 v67, v68, v69
	v_cvt_pk_bf16_f32 v68, v70, v71
	v_cvt_pk_bf16_f32 v69, v72, v73
	global_store_dwordx4 v114, v[66:69], s[26:27]
	v_cvt_pk_bf16_f32 v74, v74, v75
	v_cvt_pk_bf16_f32 v75, v76, v77
	v_cvt_pk_bf16_f32 v76, v78, v79
	v_cvt_pk_bf16_f32 v77, v80, v81
	global_store_dwordx4 v114, v[74:77], s[26:27] offset:64
	s_add_u32 s26, s26, 0x5a000
	s_addc_u32 s27, s27, 0
	v_mul_f32_e32 v132, v48, v48
	v_mul_f32_e32 v133, v49, v49
	v_mul_f32_e32 v134, v56, v56
	v_mul_f32_e32 v135, v57, v57
	v_fma_f32 v132, v50, v50, v132
	v_fma_f32 v133, v51, v51, v133
	v_fma_f32 v134, v58, v58, v134
	v_fma_f32 v135, v59, v59, v135
	v_fma_f32 v132, v52, v52, v132
	v_fma_f32 v133, v53, v53, v133
	v_fma_f32 v134, v60, v60, v134
	v_fma_f32 v135, v61, v61, v135
	v_fma_f32 v132, v54, v54, v132
	v_fma_f32 v133, v55, v55, v133
	v_fma_f32 v134, v62, v62, v134
	v_fma_f32 v135, v63, v63, v135
	v_add_f32_e32 v132, v132, v134
	v_add_f32_e32 v133, v133, v135
	s_nop 0
	v_add_f32_e32 v194, v132, v133
	ds_swizzle_b32 v195, v194 offset:swizzle(SWAP,16)
	s_waitcnt lgkmcnt(0)
	v_add_f32_e32 v194, v194, v195
	v_mov_b32_e32 v195, v194
	s_nop 1
	v_permlane32_swap_b32_e32 v194, v195
	v_add_f32_e32 v194, v194, v195
	v_fmamk_f32 v194, v194, 0x3c800000, v192
	v_rsq_f32_e32 v194, v194
	s_nop 0
	v_mul_f32_e32 v196, v146, v194
	v_mul_f32_e32 v48, v48, v196
	v_mul_f32_e32 v49, v49, v196
	v_mul_f32_e32 v50, v50, v196
	v_mul_f32_e32 v51, v51, v196
	v_mul_f32_e32 v52, v52, v196
	v_mul_f32_e32 v53, v53, v196
	v_mul_f32_e32 v54, v54, v196
	v_mul_f32_e32 v55, v55, v196
	v_mul_f32_e32 v56, v56, v196
	v_mul_f32_e32 v57, v57, v196
	v_mul_f32_e32 v58, v58, v196
	v_mul_f32_e32 v59, v59, v196
	v_mul_f32_e32 v60, v60, v196
	v_mul_f32_e32 v61, v61, v196
	v_mul_f32_e32 v62, v62, v196
	v_mul_f32_e32 v63, v63, v196
	v_mul_f32_e32 v48, v148, v48
	v_mul_f32_e32 v49, v149, v49
	v_mul_f32_e32 v50, v150, v50
	v_mul_f32_e32 v51, v151, v51
	v_mul_f32_e32 v52, v152, v52
	v_mul_f32_e32 v53, v153, v53
	v_mul_f32_e32 v54, v154, v54
	v_mul_f32_e32 v55, v155, v55
	v_mul_f32_e32 v56, v156, v56
	v_mul_f32_e32 v57, v157, v57
	v_mul_f32_e32 v58, v158, v58
	v_mul_f32_e32 v59, v159, v59
	v_mul_f32_e32 v60, v160, v60
	v_mul_f32_e32 v61, v161, v61
	v_mul_f32_e32 v62, v162, v62
	v_mul_f32_e32 v63, v163, v63
	s_waitcnt vmcnt(6)
	v_mul_f32_e32 v226, v48, v172
	v_mul_f32_e32 v227, v49, v173
	v_mul_f32_e32 v228, v50, v174
	v_mul_f32_e32 v229, v51, v175
	v_mul_f32_e32 v230, v52, v176
	v_mul_f32_e32 v231, v53, v177
	v_mul_f32_e32 v232, v54, v178
	v_mul_f32_e32 v233, v55, v179
	v_mov_b64_e32 v[244:245], v[226:227]
	v_mov_b64_e32 v[246:247], v[228:229]
	v_mov_b64_e32 v[248:249], v[230:231]
	v_mov_b64_e32 v[250:251], v[232:233]
	v_permlane32_swap_b32_e32 v226, v244
	v_permlane32_swap_b32_e32 v227, v245
	v_permlane32_swap_b32_e32 v228, v246
	v_permlane32_swap_b32_e32 v229, v247
	v_permlane32_swap_b32_e32 v230, v248
	v_permlane32_swap_b32_e32 v231, v249
	v_permlane32_swap_b32_e32 v232, v250
	v_permlane32_swap_b32_e32 v233, v251
	v_cndmask_b32_e64 v244, v226, -v244, s[36:37]
	v_cndmask_b32_e64 v245, v227, -v245, s[36:37]
	v_cndmask_b32_e64 v246, v228, -v246, s[36:37]
	v_cndmask_b32_e64 v247, v229, -v247, s[36:37]
	v_cndmask_b32_e64 v248, v230, -v248, s[36:37]
	v_cndmask_b32_e64 v249, v231, -v249, s[36:37]
	v_cndmask_b32_e64 v250, v232, -v250, s[36:37]
	v_cndmask_b32_e64 v251, v233, -v251, s[36:37]
	v_fma_f32 v48, v48, v164, v244
	v_fma_f32 v49, v49, v165, v245
	v_fma_f32 v50, v50, v166, v246
	v_fma_f32 v51, v51, v167, v247
	v_fma_f32 v52, v52, v168, v248
	v_fma_f32 v53, v53, v169, v249
	v_fma_f32 v54, v54, v170, v250
	v_fma_f32 v55, v55, v171, v251
	v_mul_f32_e32 v226, v56, v202
	v_mul_f32_e32 v227, v57, v203
	v_mul_f32_e32 v228, v58, v204
	v_mul_f32_e32 v229, v59, v205
	v_mul_f32_e32 v230, v60, v206
	v_mul_f32_e32 v231, v61, v207
	v_mul_f32_e32 v232, v62, v208
	v_mul_f32_e32 v233, v63, v209
	v_mov_b64_e32 v[244:245], v[226:227]
	v_mov_b64_e32 v[246:247], v[228:229]
	v_mov_b64_e32 v[248:249], v[230:231]
	v_mov_b64_e32 v[250:251], v[232:233]
	v_permlane32_swap_b32_e32 v226, v244
	v_permlane32_swap_b32_e32 v227, v245
	v_permlane32_swap_b32_e32 v228, v246
	v_permlane32_swap_b32_e32 v229, v247
	v_permlane32_swap_b32_e32 v230, v248
	v_permlane32_swap_b32_e32 v231, v249
	v_permlane32_swap_b32_e32 v232, v250
	v_permlane32_swap_b32_e32 v233, v251
	v_cndmask_b32_e64 v244, v226, -v244, s[36:37]
	v_cndmask_b32_e64 v245, v227, -v245, s[36:37]
	v_cndmask_b32_e64 v246, v228, -v246, s[36:37]
	v_cndmask_b32_e64 v247, v229, -v247, s[36:37]
	v_cndmask_b32_e64 v248, v230, -v248, s[36:37]
	v_cndmask_b32_e64 v249, v231, -v249, s[36:37]
	v_cndmask_b32_e64 v250, v232, -v250, s[36:37]
	v_cndmask_b32_e64 v251, v233, -v251, s[36:37]
	v_fma_f32 v56, v56, v180, v244
	v_fma_f32 v57, v57, v181, v245
	v_fma_f32 v58, v58, v182, v246
	v_fma_f32 v59, v59, v183, v247
	v_fma_f32 v60, v60, v184, v248
	v_fma_f32 v61, v61, v185, v249
	v_fma_f32 v62, v62, v186, v250
	v_fma_f32 v63, v63, v187, v251
	global_load_dwordx4 v[180:183], v136, s[6:7] offset:2048
	global_load_dwordx4 v[184:187], v136, s[6:7] offset:2064
	global_load_dwordx4 v[202:205], v137, s[6:7] offset:2048
	global_load_dwordx4 v[206:209], v137, s[6:7] offset:2064
	v_cvt_pk_bf16_f32 v48, v48, v49
	v_cvt_pk_bf16_f32 v49, v50, v51
	v_cvt_pk_bf16_f32 v50, v52, v53
	v_cvt_pk_bf16_f32 v51, v54, v55
	global_store_dwordx4 v114, v[48:51], s[26:27]
	v_cvt_pk_bf16_f32 v56, v56, v57
	v_cvt_pk_bf16_f32 v57, v58, v59
	v_cvt_pk_bf16_f32 v58, v60, v61
	v_cvt_pk_bf16_f32 v59, v62, v63
	global_store_dwordx4 v114, v[56:59], s[26:27] offset:64
	s_add_u32 s26, s26, 0x12000
	s_addc_u32 s27, s27, 0
	v_mul_f32_e32 v132, v32, v32
	v_mul_f32_e32 v133, v33, v33
	v_mul_f32_e32 v134, v40, v40
	v_mul_f32_e32 v135, v41, v41
	v_fma_f32 v132, v34, v34, v132
	v_fma_f32 v133, v35, v35, v133
	v_fma_f32 v134, v42, v42, v134
	v_fma_f32 v135, v43, v43, v135
	v_fma_f32 v132, v36, v36, v132
	v_fma_f32 v133, v37, v37, v133
	v_fma_f32 v134, v44, v44, v134
	v_fma_f32 v135, v45, v45, v135
	v_fma_f32 v132, v38, v38, v132
	v_fma_f32 v133, v39, v39, v133
	v_fma_f32 v134, v46, v46, v134
	v_fma_f32 v135, v47, v47, v135
	v_add_f32_e32 v132, v132, v134
	v_add_f32_e32 v133, v133, v135
	s_nop 0
	v_add_f32_e32 v194, v132, v133
	ds_swizzle_b32 v195, v194 offset:swizzle(SWAP,16)
	s_waitcnt lgkmcnt(0)
	v_add_f32_e32 v194, v194, v195
	v_mov_b32_e32 v195, v194
	s_nop 1
	v_permlane32_swap_b32_e32 v194, v195
	v_add_f32_e32 v194, v194, v195
	v_fmamk_f32 v194, v194, 0x3c800000, v192
	v_rsq_f32_e32 v194, v194
	s_nop 0
	v_mul_f32_e32 v196, v146, v194
	v_mul_f32_e32 v32, v32, v196
	v_mul_f32_e32 v33, v33, v196
	v_mul_f32_e32 v34, v34, v196
	v_mul_f32_e32 v35, v35, v196
	v_mul_f32_e32 v36, v36, v196
	v_mul_f32_e32 v37, v37, v196
	v_mul_f32_e32 v38, v38, v196
	v_mul_f32_e32 v39, v39, v196
	v_mul_f32_e32 v40, v40, v196
	v_mul_f32_e32 v41, v41, v196
	v_mul_f32_e32 v42, v42, v196
	v_mul_f32_e32 v43, v43, v196
	v_mul_f32_e32 v44, v44, v196
	v_mul_f32_e32 v45, v45, v196
	v_mul_f32_e32 v46, v46, v196
	v_mul_f32_e32 v47, v47, v196
	v_mul_f32_e32 v32, v148, v32
	v_mul_f32_e32 v33, v149, v33
	v_mul_f32_e32 v34, v150, v34
	v_mul_f32_e32 v35, v151, v35
	v_mul_f32_e32 v36, v152, v36
	v_mul_f32_e32 v37, v153, v37
	v_mul_f32_e32 v38, v154, v38
	v_mul_f32_e32 v39, v155, v39
	v_mul_f32_e32 v40, v156, v40
	v_mul_f32_e32 v41, v157, v41
	v_mul_f32_e32 v42, v158, v42
	v_mul_f32_e32 v43, v159, v43
	v_mul_f32_e32 v44, v160, v44
	v_mul_f32_e32 v45, v161, v45
	v_mul_f32_e32 v46, v162, v46
	v_mul_f32_e32 v47, v163, v47
	v_mul_f32_e32 v226, v32, v172
	v_mul_f32_e32 v227, v33, v173
	v_mul_f32_e32 v228, v34, v174
	v_mul_f32_e32 v229, v35, v175
	v_mul_f32_e32 v230, v36, v176
	v_mul_f32_e32 v231, v37, v177
	v_mul_f32_e32 v232, v38, v178
	v_mul_f32_e32 v233, v39, v179
	v_mov_b64_e32 v[244:245], v[226:227]
	v_mov_b64_e32 v[246:247], v[228:229]
	v_mov_b64_e32 v[248:249], v[230:231]
	v_mov_b64_e32 v[250:251], v[232:233]
	v_permlane32_swap_b32_e32 v226, v244
	v_permlane32_swap_b32_e32 v227, v245
	v_permlane32_swap_b32_e32 v228, v246
	v_permlane32_swap_b32_e32 v229, v247
	v_permlane32_swap_b32_e32 v230, v248
	v_permlane32_swap_b32_e32 v231, v249
	v_permlane32_swap_b32_e32 v232, v250
	v_permlane32_swap_b32_e32 v233, v251
	v_cndmask_b32_e64 v244, v226, -v244, s[36:37]
	v_cndmask_b32_e64 v245, v227, -v245, s[36:37]
	v_cndmask_b32_e64 v246, v228, -v246, s[36:37]
	v_cndmask_b32_e64 v247, v229, -v247, s[36:37]
	v_cndmask_b32_e64 v248, v230, -v248, s[36:37]
	v_cndmask_b32_e64 v249, v231, -v249, s[36:37]
	v_cndmask_b32_e64 v250, v232, -v250, s[36:37]
	v_cndmask_b32_e64 v251, v233, -v251, s[36:37]
	v_fma_f32 v32, v32, v164, v244
	v_fma_f32 v33, v33, v165, v245
	v_fma_f32 v34, v34, v166, v246
	v_fma_f32 v35, v35, v167, v247
	v_fma_f32 v36, v36, v168, v248
	v_fma_f32 v37, v37, v169, v249
	v_fma_f32 v38, v38, v170, v250
	v_fma_f32 v39, v39, v171, v251
	s_waitcnt vmcnt(8)
	v_mul_f32_e32 v226, v40, v218
	v_mul_f32_e32 v227, v41, v219
	v_mul_f32_e32 v228, v42, v220
	v_mul_f32_e32 v229, v43, v221
	v_mul_f32_e32 v230, v44, v222
	v_mul_f32_e32 v231, v45, v223
	v_mul_f32_e32 v232, v46, v224
	v_mul_f32_e32 v233, v47, v225
	v_mov_b64_e32 v[244:245], v[226:227]
	v_mov_b64_e32 v[246:247], v[228:229]
	v_mov_b64_e32 v[248:249], v[230:231]
	v_mov_b64_e32 v[250:251], v[232:233]
	v_permlane32_swap_b32_e32 v226, v244
	v_permlane32_swap_b32_e32 v227, v245
	v_permlane32_swap_b32_e32 v228, v246
	v_permlane32_swap_b32_e32 v229, v247
	v_permlane32_swap_b32_e32 v230, v248
	v_permlane32_swap_b32_e32 v231, v249
	v_permlane32_swap_b32_e32 v232, v250
	v_permlane32_swap_b32_e32 v233, v251
	v_cndmask_b32_e64 v244, v226, -v244, s[36:37]
	v_cndmask_b32_e64 v245, v227, -v245, s[36:37]
	v_cndmask_b32_e64 v246, v228, -v246, s[36:37]
	v_cndmask_b32_e64 v247, v229, -v247, s[36:37]
	v_cndmask_b32_e64 v248, v230, -v248, s[36:37]
	v_cndmask_b32_e64 v249, v231, -v249, s[36:37]
	v_cndmask_b32_e64 v250, v232, -v250, s[36:37]
	v_cndmask_b32_e64 v251, v233, -v251, s[36:37]
	v_fma_f32 v40, v40, v210, v244
	v_fma_f32 v41, v41, v211, v245
	v_fma_f32 v42, v42, v212, v246
	v_fma_f32 v43, v43, v213, v247
	v_fma_f32 v44, v44, v214, v248
	v_fma_f32 v45, v45, v215, v249
	v_fma_f32 v46, v46, v216, v250
	v_fma_f32 v47, v47, v217, v251
	global_load_dwordx4 v[210:213], v136, s[6:7] offset:3072
	global_load_dwordx4 v[214:217], v136, s[6:7] offset:3088
	global_load_dwordx4 v[218:221], v137, s[6:7] offset:3072
	global_load_dwordx4 v[222:225], v137, s[6:7] offset:3088
	v_cvt_pk_bf16_f32 v32, v32, v33
	v_cvt_pk_bf16_f32 v33, v34, v35
	v_cvt_pk_bf16_f32 v34, v36, v37
	v_cvt_pk_bf16_f32 v35, v38, v39
	global_store_dwordx4 v114, v[32:35], s[26:27]
	v_cvt_pk_bf16_f32 v40, v40, v41
	v_cvt_pk_bf16_f32 v41, v42, v43
	v_cvt_pk_bf16_f32 v42, v44, v45
	v_cvt_pk_bf16_f32 v43, v46, v47
	global_store_dwordx4 v114, v[40:43], s[26:27] offset:64
	s_add_u32 s26, s26, 0x12000
	s_addc_u32 s27, s27, 0
	v_mul_f32_e32 v132, v16, v16
	v_mul_f32_e32 v133, v17, v17
	v_mul_f32_e32 v134, v24, v24
	v_mul_f32_e32 v135, v25, v25
	v_fma_f32 v132, v18, v18, v132
	v_fma_f32 v133, v19, v19, v133
	v_fma_f32 v134, v26, v26, v134
	v_fma_f32 v135, v27, v27, v135
	v_fma_f32 v132, v20, v20, v132
	v_fma_f32 v133, v21, v21, v133
	v_fma_f32 v134, v28, v28, v134
	v_fma_f32 v135, v29, v29, v135
	v_fma_f32 v132, v22, v22, v132
	v_fma_f32 v133, v23, v23, v133
	v_fma_f32 v134, v30, v30, v134
	v_fma_f32 v135, v31, v31, v135
	v_add_f32_e32 v132, v132, v134
	v_add_f32_e32 v133, v133, v135
	s_nop 0
	v_add_f32_e32 v194, v132, v133
	ds_swizzle_b32 v195, v194 offset:swizzle(SWAP,16)
	s_waitcnt lgkmcnt(0)
	v_add_f32_e32 v194, v194, v195
	v_mov_b32_e32 v195, v194
	s_nop 1
	v_permlane32_swap_b32_e32 v194, v195
	v_add_f32_e32 v194, v194, v195
	v_fmamk_f32 v194, v194, 0x3c800000, v192
	v_rsq_f32_e32 v194, v194
	s_nop 0
	v_mul_f32_e32 v196, v146, v194
	v_mul_f32_e32 v16, v16, v196
	v_mul_f32_e32 v17, v17, v196
	v_mul_f32_e32 v18, v18, v196
	v_mul_f32_e32 v19, v19, v196
	v_mul_f32_e32 v20, v20, v196
	v_mul_f32_e32 v21, v21, v196
	v_mul_f32_e32 v22, v22, v196
	v_mul_f32_e32 v23, v23, v196
	v_mul_f32_e32 v24, v24, v196
	v_mul_f32_e32 v25, v25, v196
	v_mul_f32_e32 v26, v26, v196
	v_mul_f32_e32 v27, v27, v196
	v_mul_f32_e32 v28, v28, v196
	v_mul_f32_e32 v29, v29, v196
	v_mul_f32_e32 v30, v30, v196
	v_mul_f32_e32 v31, v31, v196
	v_mul_f32_e32 v16, v148, v16
	v_mul_f32_e32 v17, v149, v17
	v_mul_f32_e32 v18, v150, v18
	v_mul_f32_e32 v19, v151, v19
	v_mul_f32_e32 v20, v152, v20
	v_mul_f32_e32 v21, v153, v21
	v_mul_f32_e32 v22, v154, v22
	v_mul_f32_e32 v23, v155, v23
	v_mul_f32_e32 v24, v156, v24
	v_mul_f32_e32 v25, v157, v25
	v_mul_f32_e32 v26, v158, v26
	v_mul_f32_e32 v27, v159, v27
	v_mul_f32_e32 v28, v160, v28
	v_mul_f32_e32 v29, v161, v29
	v_mul_f32_e32 v30, v162, v30
	v_mul_f32_e32 v31, v163, v31
	v_mul_f32_e32 v226, v16, v172
	v_mul_f32_e32 v227, v17, v173
	v_mul_f32_e32 v228, v18, v174
	v_mul_f32_e32 v229, v19, v175
	v_mul_f32_e32 v230, v20, v176
	v_mul_f32_e32 v231, v21, v177
	v_mul_f32_e32 v232, v22, v178
	v_mul_f32_e32 v233, v23, v179
	v_mov_b64_e32 v[244:245], v[226:227]
	v_mov_b64_e32 v[246:247], v[228:229]
	v_mov_b64_e32 v[248:249], v[230:231]
	v_mov_b64_e32 v[250:251], v[232:233]
	v_permlane32_swap_b32_e32 v226, v244
	v_permlane32_swap_b32_e32 v227, v245
	v_permlane32_swap_b32_e32 v228, v246
	v_permlane32_swap_b32_e32 v229, v247
	v_permlane32_swap_b32_e32 v230, v248
	v_permlane32_swap_b32_e32 v231, v249
	v_permlane32_swap_b32_e32 v232, v250
	v_permlane32_swap_b32_e32 v233, v251
	v_cndmask_b32_e64 v244, v226, -v244, s[36:37]
	v_cndmask_b32_e64 v245, v227, -v245, s[36:37]
	v_cndmask_b32_e64 v246, v228, -v246, s[36:37]
	v_cndmask_b32_e64 v247, v229, -v247, s[36:37]
	v_cndmask_b32_e64 v248, v230, -v248, s[36:37]
	v_cndmask_b32_e64 v249, v231, -v249, s[36:37]
	v_cndmask_b32_e64 v250, v232, -v250, s[36:37]
	v_cndmask_b32_e64 v251, v233, -v251, s[36:37]
	v_fma_f32 v16, v16, v164, v244
	v_fma_f32 v17, v17, v165, v245
	v_fma_f32 v18, v18, v166, v246
	v_fma_f32 v19, v19, v167, v247
	v_fma_f32 v20, v20, v168, v248
	v_fma_f32 v21, v21, v169, v249
	v_fma_f32 v22, v22, v170, v250
	v_fma_f32 v23, v23, v171, v251
	s_waitcnt vmcnt(8)
	v_mul_f32_e32 v226, v24, v202
	v_mul_f32_e32 v227, v25, v203
	v_mul_f32_e32 v228, v26, v204
	v_mul_f32_e32 v229, v27, v205
	v_mul_f32_e32 v230, v28, v206
	v_mul_f32_e32 v231, v29, v207
	v_mul_f32_e32 v232, v30, v208
	v_mul_f32_e32 v233, v31, v209
	v_mov_b64_e32 v[244:245], v[226:227]
	v_mov_b64_e32 v[246:247], v[228:229]
	v_mov_b64_e32 v[248:249], v[230:231]
	v_mov_b64_e32 v[250:251], v[232:233]
	v_permlane32_swap_b32_e32 v226, v244
	v_permlane32_swap_b32_e32 v227, v245
	v_permlane32_swap_b32_e32 v228, v246
	v_permlane32_swap_b32_e32 v229, v247
	v_permlane32_swap_b32_e32 v230, v248
	v_permlane32_swap_b32_e32 v231, v249
	v_permlane32_swap_b32_e32 v232, v250
	v_permlane32_swap_b32_e32 v233, v251
	v_cndmask_b32_e64 v244, v226, -v244, s[36:37]
	v_cndmask_b32_e64 v245, v227, -v245, s[36:37]
	v_cndmask_b32_e64 v246, v228, -v246, s[36:37]
	v_cndmask_b32_e64 v247, v229, -v247, s[36:37]
	v_cndmask_b32_e64 v248, v230, -v248, s[36:37]
	v_cndmask_b32_e64 v249, v231, -v249, s[36:37]
	v_cndmask_b32_e64 v250, v232, -v250, s[36:37]
	v_cndmask_b32_e64 v251, v233, -v251, s[36:37]
	v_fma_f32 v24, v24, v180, v244
	v_fma_f32 v25, v25, v181, v245
	v_fma_f32 v26, v26, v182, v246
	v_fma_f32 v27, v27, v183, v247
	v_fma_f32 v28, v28, v184, v248
	v_fma_f32 v29, v29, v185, v249
	v_fma_f32 v30, v30, v186, v250
	v_fma_f32 v31, v31, v187, v251
	v_cvt_pk_bf16_f32 v16, v16, v17
	v_cvt_pk_bf16_f32 v17, v18, v19
	v_cvt_pk_bf16_f32 v18, v20, v21
	v_cvt_pk_bf16_f32 v19, v22, v23
	global_store_dwordx4 v114, v[16:19], s[26:27]
	v_cvt_pk_bf16_f32 v24, v24, v25
	v_cvt_pk_bf16_f32 v25, v26, v27
	v_cvt_pk_bf16_f32 v26, v28, v29
	v_cvt_pk_bf16_f32 v27, v30, v31
	global_store_dwordx4 v114, v[24:27], s[26:27] offset:64
	s_add_u32 s26, s26, 0x12000
	s_addc_u32 s27, s27, 0
	v_mul_f32_e32 v132, v0, v0
	v_mul_f32_e32 v133, v1, v1
	v_mul_f32_e32 v134, v8, v8
	v_mul_f32_e32 v135, v9, v9
	v_fma_f32 v132, v2, v2, v132
	v_fma_f32 v133, v3, v3, v133
	v_fma_f32 v134, v10, v10, v134
	v_fma_f32 v135, v11, v11, v135
	v_fma_f32 v132, v4, v4, v132
	v_fma_f32 v133, v5, v5, v133
	v_fma_f32 v134, v12, v12, v134
	v_fma_f32 v135, v13, v13, v135
	v_fma_f32 v132, v6, v6, v132
	v_fma_f32 v133, v7, v7, v133
	v_fma_f32 v134, v14, v14, v134
	v_fma_f32 v135, v15, v15, v135
	v_add_f32_e32 v132, v132, v134
	v_add_f32_e32 v133, v133, v135
	s_nop 0
	v_add_f32_e32 v194, v132, v133
	ds_swizzle_b32 v195, v194 offset:swizzle(SWAP,16)
	s_waitcnt lgkmcnt(0)
	v_add_f32_e32 v194, v194, v195
	v_mov_b32_e32 v195, v194
	s_nop 1
	v_permlane32_swap_b32_e32 v194, v195
	v_add_f32_e32 v194, v194, v195
	v_fmamk_f32 v194, v194, 0x3c800000, v192
	v_rsq_f32_e32 v194, v194
	s_nop 0
	v_mul_f32_e32 v196, v146, v194
	v_mul_f32_e32 v0, v0, v196
	v_mul_f32_e32 v1, v1, v196
	v_mul_f32_e32 v2, v2, v196
	v_mul_f32_e32 v3, v3, v196
	v_mul_f32_e32 v4, v4, v196
	v_mul_f32_e32 v5, v5, v196
	v_mul_f32_e32 v6, v6, v196
	v_mul_f32_e32 v7, v7, v196
	v_mul_f32_e32 v8, v8, v196
	v_mul_f32_e32 v9, v9, v196
	v_mul_f32_e32 v10, v10, v196
	v_mul_f32_e32 v11, v11, v196
	v_mul_f32_e32 v12, v12, v196
	v_mul_f32_e32 v13, v13, v196
	v_mul_f32_e32 v14, v14, v196
	v_mul_f32_e32 v15, v15, v196
	v_mul_f32_e32 v0, v148, v0
	v_mul_f32_e32 v1, v149, v1
	v_mul_f32_e32 v2, v150, v2
	v_mul_f32_e32 v3, v151, v3
	v_mul_f32_e32 v4, v152, v4
	v_mul_f32_e32 v5, v153, v5
	v_mul_f32_e32 v6, v154, v6
	v_mul_f32_e32 v7, v155, v7
	v_mul_f32_e32 v8, v156, v8
	v_mul_f32_e32 v9, v157, v9
	v_mul_f32_e32 v10, v158, v10
	v_mul_f32_e32 v11, v159, v11
	v_mul_f32_e32 v12, v160, v12
	v_mul_f32_e32 v13, v161, v13
	v_mul_f32_e32 v14, v162, v14
	v_mul_f32_e32 v15, v163, v15
	v_mul_f32_e32 v226, v0, v172
	v_mul_f32_e32 v227, v1, v173
	v_mul_f32_e32 v228, v2, v174
	v_mul_f32_e32 v229, v3, v175
	v_mul_f32_e32 v230, v4, v176
	v_mul_f32_e32 v231, v5, v177
	v_mul_f32_e32 v232, v6, v178
	v_mul_f32_e32 v233, v7, v179
	v_mov_b64_e32 v[244:245], v[226:227]
	v_mov_b64_e32 v[246:247], v[228:229]
	v_mov_b64_e32 v[248:249], v[230:231]
	v_mov_b64_e32 v[250:251], v[232:233]
	v_permlane32_swap_b32_e32 v226, v244
	v_permlane32_swap_b32_e32 v227, v245
	v_permlane32_swap_b32_e32 v228, v246
	v_permlane32_swap_b32_e32 v229, v247
	v_permlane32_swap_b32_e32 v230, v248
	v_permlane32_swap_b32_e32 v231, v249
	v_permlane32_swap_b32_e32 v232, v250
	v_permlane32_swap_b32_e32 v233, v251
	v_cndmask_b32_e64 v244, v226, -v244, s[36:37]
	v_cndmask_b32_e64 v245, v227, -v245, s[36:37]
	v_cndmask_b32_e64 v246, v228, -v246, s[36:37]
	v_cndmask_b32_e64 v247, v229, -v247, s[36:37]
	v_cndmask_b32_e64 v248, v230, -v248, s[36:37]
	v_cndmask_b32_e64 v249, v231, -v249, s[36:37]
	v_cndmask_b32_e64 v250, v232, -v250, s[36:37]
	v_cndmask_b32_e64 v251, v233, -v251, s[36:37]
	v_fma_f32 v0, v0, v164, v244
	v_fma_f32 v1, v1, v165, v245
	v_fma_f32 v2, v2, v166, v246
	v_fma_f32 v3, v3, v167, v247
	v_fma_f32 v4, v4, v168, v248
	v_fma_f32 v5, v5, v169, v249
	v_fma_f32 v6, v6, v170, v250
	v_fma_f32 v7, v7, v171, v251
	s_waitcnt vmcnt(4)
	v_mul_f32_e32 v226, v8, v218
	v_mul_f32_e32 v227, v9, v219
	v_mul_f32_e32 v228, v10, v220
	v_mul_f32_e32 v229, v11, v221
	v_mul_f32_e32 v230, v12, v222
	v_mul_f32_e32 v231, v13, v223
	v_mul_f32_e32 v232, v14, v224
	v_mul_f32_e32 v233, v15, v225
	v_mov_b64_e32 v[244:245], v[226:227]
	v_mov_b64_e32 v[246:247], v[228:229]
	v_mov_b64_e32 v[248:249], v[230:231]
	v_mov_b64_e32 v[250:251], v[232:233]
	v_permlane32_swap_b32_e32 v226, v244
	v_permlane32_swap_b32_e32 v227, v245
	v_permlane32_swap_b32_e32 v228, v246
	v_permlane32_swap_b32_e32 v229, v247
	v_permlane32_swap_b32_e32 v230, v248
	v_permlane32_swap_b32_e32 v231, v249
	v_permlane32_swap_b32_e32 v232, v250
	v_permlane32_swap_b32_e32 v233, v251
	v_cndmask_b32_e64 v244, v226, -v244, s[36:37]
	v_cndmask_b32_e64 v245, v227, -v245, s[36:37]
	v_cndmask_b32_e64 v246, v228, -v246, s[36:37]
	v_cndmask_b32_e64 v247, v229, -v247, s[36:37]
	v_cndmask_b32_e64 v248, v230, -v248, s[36:37]
	v_cndmask_b32_e64 v249, v231, -v249, s[36:37]
	v_cndmask_b32_e64 v250, v232, -v250, s[36:37]
	v_cndmask_b32_e64 v251, v233, -v251, s[36:37]
	v_fma_f32 v8, v8, v210, v244
	v_fma_f32 v9, v9, v211, v245
	v_fma_f32 v10, v10, v212, v246
	v_fma_f32 v11, v11, v213, v247
	v_fma_f32 v12, v12, v214, v248
	v_fma_f32 v13, v13, v215, v249
	v_fma_f32 v14, v14, v216, v250
	v_fma_f32 v15, v15, v217, v251
	v_cvt_pk_bf16_f32 v0, v0, v1
	v_cvt_pk_bf16_f32 v1, v2, v3
	v_cvt_pk_bf16_f32 v2, v4, v5
	v_cvt_pk_bf16_f32 v3, v6, v7
	global_store_dwordx4 v114, v[0:3], s[26:27]
	v_cvt_pk_bf16_f32 v8, v8, v9
	v_cvt_pk_bf16_f32 v9, v10, v11
	v_cvt_pk_bf16_f32 v10, v12, v13
	v_cvt_pk_bf16_f32 v11, v14, v15
	global_store_dwordx4 v114, v[8:11], s[26:27] offset:64
	s_branch .Lqkv_epi_done
.Lqkv_epi_norope:
	v_mul_f32_e32 v132, v116, v116
	v_mul_f32_e32 v133, v117, v117
	v_mul_f32_e32 v134, v124, v124
	v_mul_f32_e32 v135, v125, v125
	v_fma_f32 v132, v118, v118, v132
	v_fma_f32 v133, v119, v119, v133
	v_fma_f32 v134, v126, v126, v134
	v_fma_f32 v135, v127, v127, v135
	v_fma_f32 v132, v120, v120, v132
	v_fma_f32 v133, v121, v121, v133
	v_fma_f32 v134, v128, v128, v134
	v_fma_f32 v135, v129, v129, v135
	v_fma_f32 v132, v122, v122, v132
	v_fma_f32 v133, v123, v123, v133
	v_fma_f32 v134, v130, v130, v134
	v_fma_f32 v135, v131, v131, v135
	v_add_f32_e32 v132, v132, v134
	v_add_f32_e32 v133, v133, v135
	s_nop 0
	v_add_f32_e32 v194, v132, v133
	ds_swizzle_b32 v195, v194 offset:swizzle(SWAP,16)
	s_waitcnt lgkmcnt(0)
	v_add_f32_e32 v194, v194, v195
	v_mov_b32_e32 v195, v194
	s_nop 1
	v_permlane32_swap_b32_e32 v194, v195
	v_add_f32_e32 v194, v194, v195
	v_fmamk_f32 v194, v194, 0x3c800000, v192
	v_rsq_f32_e32 v194, v194
	s_nop 0
	v_mul_f32_e32 v196, v146, v194
	v_mul_f32_e32 v116, v116, v196
	v_mul_f32_e32 v117, v117, v196
	v_mul_f32_e32 v118, v118, v196
	v_mul_f32_e32 v119, v119, v196
	v_mul_f32_e32 v120, v120, v196
	v_mul_f32_e32 v121, v121, v196
	v_mul_f32_e32 v122, v122, v196
	v_mul_f32_e32 v123, v123, v196
	v_mul_f32_e32 v124, v124, v196
	v_mul_f32_e32 v125, v125, v196
	v_mul_f32_e32 v126, v126, v196
	v_mul_f32_e32 v127, v127, v196
	v_mul_f32_e32 v128, v128, v196
	v_mul_f32_e32 v129, v129, v196
	v_mul_f32_e32 v130, v130, v196
	v_mul_f32_e32 v131, v131, v196
	s_waitcnt vmcnt(0)
	v_mul_f32_e32 v116, v148, v116
	v_mul_f32_e32 v117, v149, v117
	v_mul_f32_e32 v118, v150, v118
	v_mul_f32_e32 v119, v151, v119
	v_mul_f32_e32 v120, v152, v120
	v_mul_f32_e32 v121, v153, v121
	v_mul_f32_e32 v122, v154, v122
	v_mul_f32_e32 v123, v155, v123
	v_mul_f32_e32 v124, v156, v124
	v_mul_f32_e32 v125, v157, v125
	v_mul_f32_e32 v126, v158, v126
	v_mul_f32_e32 v127, v159, v127
	v_mul_f32_e32 v128, v160, v128
	v_mul_f32_e32 v129, v161, v129
	v_mul_f32_e32 v130, v162, v130
	v_mul_f32_e32 v131, v163, v131
	v_cvt_pk_bf16_f32 v116, v116, v117
	v_cvt_pk_bf16_f32 v117, v118, v119
	v_cvt_pk_bf16_f32 v118, v120, v121
	v_cvt_pk_bf16_f32 v119, v122, v123
	global_store_dwordx4 v114, v[116:119], s[26:27]
	v_cvt_pk_bf16_f32 v124, v124, v125
	v_cvt_pk_bf16_f32 v125, v126, v127
	v_cvt_pk_bf16_f32 v126, v128, v129
	v_cvt_pk_bf16_f32 v127, v130, v131
	global_store_dwordx4 v114, v[124:127], s[26:27] offset:64
	s_add_u32 s26, s26, 0x12000
	s_addc_u32 s27, s27, 0
	v_mul_f32_e32 v132, v98, v98
	v_mul_f32_e32 v133, v99, v99
	v_mul_f32_e32 v134, v106, v106
	v_mul_f32_e32 v135, v107, v107
	v_fma_f32 v132, v100, v100, v132
	v_fma_f32 v133, v101, v101, v133
	v_fma_f32 v134, v108, v108, v134
	v_fma_f32 v135, v109, v109, v135
	v_fma_f32 v132, v102, v102, v132
	v_fma_f32 v133, v103, v103, v133
	v_fma_f32 v134, v110, v110, v134
	v_fma_f32 v135, v111, v111, v135
	v_fma_f32 v132, v104, v104, v132
	v_fma_f32 v133, v105, v105, v133
	v_fma_f32 v134, v112, v112, v134
	v_fma_f32 v135, v113, v113, v135
	v_add_f32_e32 v132, v132, v134
	v_add_f32_e32 v133, v133, v135
	s_nop 0
	v_add_f32_e32 v194, v132, v133
	ds_swizzle_b32 v195, v194 offset:swizzle(SWAP,16)
	s_waitcnt lgkmcnt(0)
	v_add_f32_e32 v194, v194, v195
	v_mov_b32_e32 v195, v194
	s_nop 1
	v_permlane32_swap_b32_e32 v194, v195
	v_add_f32_e32 v194, v194, v195
	v_fmamk_f32 v194, v194, 0x3c800000, v192
	v_rsq_f32_e32 v194, v194
	s_nop 0
	v_mul_f32_e32 v196, v146, v194
	v_mul_f32_e32 v98, v98, v196
	v_mul_f32_e32 v99, v99, v196
	v_mul_f32_e32 v100, v100, v196
	v_mul_f32_e32 v101, v101, v196
	v_mul_f32_e32 v102, v102, v196
	v_mul_f32_e32 v103, v103, v196
	v_mul_f32_e32 v104, v104, v196
	v_mul_f32_e32 v105, v105, v196
	v_mul_f32_e32 v106, v106, v196
	v_mul_f32_e32 v107, v107, v196
	v_mul_f32_e32 v108, v108, v196
	v_mul_f32_e32 v109, v109, v196
	v_mul_f32_e32 v110, v110, v196
	v_mul_f32_e32 v111, v111, v196
	v_mul_f32_e32 v112, v112, v196
	v_mul_f32_e32 v113, v113, v196
	v_mul_f32_e32 v98, v148, v98
	v_mul_f32_e32 v99, v149, v99
	v_mul_f32_e32 v100, v150, v100
	v_mul_f32_e32 v101, v151, v101
	v_mul_f32_e32 v102, v152, v102
	v_mul_f32_e32 v103, v153, v103
	v_mul_f32_e32 v104, v154, v104
	v_mul_f32_e32 v105, v155, v105
	v_mul_f32_e32 v106, v156, v106
	v_mul_f32_e32 v107, v157, v107
	v_mul_f32_e32 v108, v158, v108
	v_mul_f32_e32 v109, v159, v109
	v_mul_f32_e32 v110, v160, v110
	v_mul_f32_e32 v111, v161, v111
	v_mul_f32_e32 v112, v162, v112
	v_mul_f32_e32 v113, v163, v113
	v_cvt_pk_bf16_f32 v98, v98, v99
	v_cvt_pk_bf16_f32 v99, v100, v101
	v_cvt_pk_bf16_f32 v100, v102, v103
	v_cvt_pk_bf16_f32 v101, v104, v105
	global_store_dwordx4 v114, v[98:101], s[26:27]
	v_cvt_pk_bf16_f32 v106, v106, v107
	v_cvt_pk_bf16_f32 v107, v108, v109
	v_cvt_pk_bf16_f32 v108, v110, v111
	v_cvt_pk_bf16_f32 v109, v112, v113
	global_store_dwordx4 v114, v[106:109], s[26:27] offset:64
	s_add_u32 s26, s26, 0x12000
	s_addc_u32 s27, s27, 0
	v_mul_f32_e32 v132, v82, v82
	v_mul_f32_e32 v133, v83, v83
	v_mul_f32_e32 v134, v90, v90
	v_mul_f32_e32 v135, v91, v91
	v_fma_f32 v132, v84, v84, v132
	v_fma_f32 v133, v85, v85, v133
	v_fma_f32 v134, v92, v92, v134
	v_fma_f32 v135, v93, v93, v135
	v_fma_f32 v132, v86, v86, v132
	v_fma_f32 v133, v87, v87, v133
	v_fma_f32 v134, v94, v94, v134
	v_fma_f32 v135, v95, v95, v135
	v_fma_f32 v132, v88, v88, v132
	v_fma_f32 v133, v89, v89, v133
	v_fma_f32 v134, v96, v96, v134
	v_fma_f32 v135, v97, v97, v135
	v_add_f32_e32 v132, v132, v134
	v_add_f32_e32 v133, v133, v135
	s_nop 0
	v_add_f32_e32 v194, v132, v133
	ds_swizzle_b32 v195, v194 offset:swizzle(SWAP,16)
	s_waitcnt lgkmcnt(0)
	v_add_f32_e32 v194, v194, v195
	v_mov_b32_e32 v195, v194
	s_nop 1
	v_permlane32_swap_b32_e32 v194, v195
	v_add_f32_e32 v194, v194, v195
	v_fmamk_f32 v194, v194, 0x3c800000, v192
	v_rsq_f32_e32 v194, v194
	s_nop 0
	v_mul_f32_e32 v196, v146, v194
	v_mul_f32_e32 v82, v82, v196
	v_mul_f32_e32 v83, v83, v196
	v_mul_f32_e32 v84, v84, v196
	v_mul_f32_e32 v85, v85, v196
	v_mul_f32_e32 v86, v86, v196
	v_mul_f32_e32 v87, v87, v196
	v_mul_f32_e32 v88, v88, v196
	v_mul_f32_e32 v89, v89, v196
	v_mul_f32_e32 v90, v90, v196
	v_mul_f32_e32 v91, v91, v196
	v_mul_f32_e32 v92, v92, v196
	v_mul_f32_e32 v93, v93, v196
	v_mul_f32_e32 v94, v94, v196
	v_mul_f32_e32 v95, v95, v196
	v_mul_f32_e32 v96, v96, v196
	v_mul_f32_e32 v97, v97, v196
	v_mul_f32_e32 v82, v148, v82
	v_mul_f32_e32 v83, v149, v83
	v_mul_f32_e32 v84, v150, v84
	v_mul_f32_e32 v85, v151, v85
	v_mul_f32_e32 v86, v152, v86
	v_mul_f32_e32 v87, v153, v87
	v_mul_f32_e32 v88, v154, v88
	v_mul_f32_e32 v89, v155, v89
	v_mul_f32_e32 v90, v156, v90
	v_mul_f32_e32 v91, v157, v91
	v_mul_f32_e32 v92, v158, v92
	v_mul_f32_e32 v93, v159, v93
	v_mul_f32_e32 v94, v160, v94
	v_mul_f32_e32 v95, v161, v95
	v_mul_f32_e32 v96, v162, v96
	v_mul_f32_e32 v97, v163, v97
	v_cvt_pk_bf16_f32 v82, v82, v83
	v_cvt_pk_bf16_f32 v83, v84, v85
	v_cvt_pk_bf16_f32 v84, v86, v87
	v_cvt_pk_bf16_f32 v85, v88, v89
	global_store_dwordx4 v114, v[82:85], s[26:27]
	v_cvt_pk_bf16_f32 v90, v90, v91
	v_cvt_pk_bf16_f32 v91, v92, v93
	v_cvt_pk_bf16_f32 v92, v94, v95
	v_cvt_pk_bf16_f32 v93, v96, v97
	global_store_dwordx4 v114, v[90:93], s[26:27] offset:64
	s_add_u32 s26, s26, 0x12000
	s_addc_u32 s27, s27, 0
	v_mul_f32_e32 v132, v66, v66
	v_mul_f32_e32 v133, v67, v67
	v_mul_f32_e32 v134, v74, v74
	v_mul_f32_e32 v135, v75, v75
	v_fma_f32 v132, v68, v68, v132
	v_fma_f32 v133, v69, v69, v133
	v_fma_f32 v134, v76, v76, v134
	v_fma_f32 v135, v77, v77, v135
	v_fma_f32 v132, v70, v70, v132
	v_fma_f32 v133, v71, v71, v133
	v_fma_f32 v134, v78, v78, v134
	v_fma_f32 v135, v79, v79, v135
	v_fma_f32 v132, v72, v72, v132
	v_fma_f32 v133, v73, v73, v133
	v_fma_f32 v134, v80, v80, v134
	v_fma_f32 v135, v81, v81, v135
	v_add_f32_e32 v132, v132, v134
	v_add_f32_e32 v133, v133, v135
	s_nop 0
	v_add_f32_e32 v194, v132, v133
	ds_swizzle_b32 v195, v194 offset:swizzle(SWAP,16)
	s_waitcnt lgkmcnt(0)
	v_add_f32_e32 v194, v194, v195
	v_mov_b32_e32 v195, v194
	s_nop 1
	v_permlane32_swap_b32_e32 v194, v195
	v_add_f32_e32 v194, v194, v195
	v_fmamk_f32 v194, v194, 0x3c800000, v192
	v_rsq_f32_e32 v194, v194
	s_nop 0
	v_mul_f32_e32 v196, v146, v194
	v_mul_f32_e32 v66, v66, v196
	v_mul_f32_e32 v67, v67, v196
	v_mul_f32_e32 v68, v68, v196
	v_mul_f32_e32 v69, v69, v196
	v_mul_f32_e32 v70, v70, v196
	v_mul_f32_e32 v71, v71, v196
	v_mul_f32_e32 v72, v72, v196
	v_mul_f32_e32 v73, v73, v196
	v_mul_f32_e32 v74, v74, v196
	v_mul_f32_e32 v75, v75, v196
	v_mul_f32_e32 v76, v76, v196
	v_mul_f32_e32 v77, v77, v196
	v_mul_f32_e32 v78, v78, v196
	v_mul_f32_e32 v79, v79, v196
	v_mul_f32_e32 v80, v80, v196
	v_mul_f32_e32 v81, v81, v196
	v_mul_f32_e32 v66, v148, v66
	v_mul_f32_e32 v67, v149, v67
	v_mul_f32_e32 v68, v150, v68
	v_mul_f32_e32 v69, v151, v69
	v_mul_f32_e32 v70, v152, v70
	v_mul_f32_e32 v71, v153, v71
	v_mul_f32_e32 v72, v154, v72
	v_mul_f32_e32 v73, v155, v73
	v_mul_f32_e32 v74, v156, v74
	v_mul_f32_e32 v75, v157, v75
	v_mul_f32_e32 v76, v158, v76
	v_mul_f32_e32 v77, v159, v77
	v_mul_f32_e32 v78, v160, v78
	v_mul_f32_e32 v79, v161, v79
	v_mul_f32_e32 v80, v162, v80
	v_mul_f32_e32 v81, v163, v81
	v_cvt_pk_bf16_f32 v66, v66, v67
	v_cvt_pk_bf16_f32 v67, v68, v69
	v_cvt_pk_bf16_f32 v68, v70, v71
	v_cvt_pk_bf16_f32 v69, v72, v73
	global_store_dwordx4 v114, v[66:69], s[26:27]
	v_cvt_pk_bf16_f32 v74, v74, v75
	v_cvt_pk_bf16_f32 v75, v76, v77
	v_cvt_pk_bf16_f32 v76, v78, v79
	v_cvt_pk_bf16_f32 v77, v80, v81
	global_store_dwordx4 v114, v[74:77], s[26:27] offset:64
	s_add_u32 s26, s26, 0x5a000
	s_addc_u32 s27, s27, 0
	v_mul_f32_e32 v132, v48, v48
	v_mul_f32_e32 v133, v49, v49
	v_mul_f32_e32 v134, v56, v56
	v_mul_f32_e32 v135, v57, v57
	v_fma_f32 v132, v50, v50, v132
	v_fma_f32 v133, v51, v51, v133
	v_fma_f32 v134, v58, v58, v134
	v_fma_f32 v135, v59, v59, v135
	v_fma_f32 v132, v52, v52, v132
	v_fma_f32 v133, v53, v53, v133
	v_fma_f32 v134, v60, v60, v134
	v_fma_f32 v135, v61, v61, v135
	v_fma_f32 v132, v54, v54, v132
	v_fma_f32 v133, v55, v55, v133
	v_fma_f32 v134, v62, v62, v134
	v_fma_f32 v135, v63, v63, v135
	v_add_f32_e32 v132, v132, v134
	v_add_f32_e32 v133, v133, v135
	s_nop 0
	v_add_f32_e32 v194, v132, v133
	ds_swizzle_b32 v195, v194 offset:swizzle(SWAP,16)
	s_waitcnt lgkmcnt(0)
	v_add_f32_e32 v194, v194, v195
	v_mov_b32_e32 v195, v194
	s_nop 1
	v_permlane32_swap_b32_e32 v194, v195
	v_add_f32_e32 v194, v194, v195
	v_fmamk_f32 v194, v194, 0x3c800000, v192
	v_rsq_f32_e32 v194, v194
	s_nop 0
	v_mul_f32_e32 v196, v146, v194
	v_mul_f32_e32 v48, v48, v196
	v_mul_f32_e32 v49, v49, v196
	v_mul_f32_e32 v50, v50, v196
	v_mul_f32_e32 v51, v51, v196
	v_mul_f32_e32 v52, v52, v196
	v_mul_f32_e32 v53, v53, v196
	v_mul_f32_e32 v54, v54, v196
	v_mul_f32_e32 v55, v55, v196
	v_mul_f32_e32 v56, v56, v196
	v_mul_f32_e32 v57, v57, v196
	v_mul_f32_e32 v58, v58, v196
	v_mul_f32_e32 v59, v59, v196
	v_mul_f32_e32 v60, v60, v196
	v_mul_f32_e32 v61, v61, v196
	v_mul_f32_e32 v62, v62, v196
	v_mul_f32_e32 v63, v63, v196
	v_mul_f32_e32 v48, v148, v48
	v_mul_f32_e32 v49, v149, v49
	v_mul_f32_e32 v50, v150, v50
	v_mul_f32_e32 v51, v151, v51
	v_mul_f32_e32 v52, v152, v52
	v_mul_f32_e32 v53, v153, v53
	v_mul_f32_e32 v54, v154, v54
	v_mul_f32_e32 v55, v155, v55
	v_mul_f32_e32 v56, v156, v56
	v_mul_f32_e32 v57, v157, v57
	v_mul_f32_e32 v58, v158, v58
	v_mul_f32_e32 v59, v159, v59
	v_mul_f32_e32 v60, v160, v60
	v_mul_f32_e32 v61, v161, v61
	v_mul_f32_e32 v62, v162, v62
	v_mul_f32_e32 v63, v163, v63
	v_cvt_pk_bf16_f32 v48, v48, v49
	v_cvt_pk_bf16_f32 v49, v50, v51
	v_cvt_pk_bf16_f32 v50, v52, v53
	v_cvt_pk_bf16_f32 v51, v54, v55
	global_store_dwordx4 v114, v[48:51], s[26:27]
	v_cvt_pk_bf16_f32 v56, v56, v57
	v_cvt_pk_bf16_f32 v57, v58, v59
	v_cvt_pk_bf16_f32 v58, v60, v61
	v_cvt_pk_bf16_f32 v59, v62, v63
	global_store_dwordx4 v114, v[56:59], s[26:27] offset:64
	s_add_u32 s26, s26, 0x12000
	s_addc_u32 s27, s27, 0
	v_mul_f32_e32 v132, v32, v32
	v_mul_f32_e32 v133, v33, v33
	v_mul_f32_e32 v134, v40, v40
	v_mul_f32_e32 v135, v41, v41
	v_fma_f32 v132, v34, v34, v132
	v_fma_f32 v133, v35, v35, v133
	v_fma_f32 v134, v42, v42, v134
	v_fma_f32 v135, v43, v43, v135
	v_fma_f32 v132, v36, v36, v132
	v_fma_f32 v133, v37, v37, v133
	v_fma_f32 v134, v44, v44, v134
	v_fma_f32 v135, v45, v45, v135
	v_fma_f32 v132, v38, v38, v132
	v_fma_f32 v133, v39, v39, v133
	v_fma_f32 v134, v46, v46, v134
	v_fma_f32 v135, v47, v47, v135
	v_add_f32_e32 v132, v132, v134
	v_add_f32_e32 v133, v133, v135
	s_nop 0
	v_add_f32_e32 v194, v132, v133
	ds_swizzle_b32 v195, v194 offset:swizzle(SWAP,16)
	s_waitcnt lgkmcnt(0)
	v_add_f32_e32 v194, v194, v195
	v_mov_b32_e32 v195, v194
	s_nop 1
	v_permlane32_swap_b32_e32 v194, v195
	v_add_f32_e32 v194, v194, v195
	v_fmamk_f32 v194, v194, 0x3c800000, v192
	v_rsq_f32_e32 v194, v194
	s_nop 0
	v_mul_f32_e32 v196, v146, v194
	v_mul_f32_e32 v32, v32, v196
	v_mul_f32_e32 v33, v33, v196
	v_mul_f32_e32 v34, v34, v196
	v_mul_f32_e32 v35, v35, v196
	v_mul_f32_e32 v36, v36, v196
	v_mul_f32_e32 v37, v37, v196
	v_mul_f32_e32 v38, v38, v196
	v_mul_f32_e32 v39, v39, v196
	v_mul_f32_e32 v40, v40, v196
	v_mul_f32_e32 v41, v41, v196
	v_mul_f32_e32 v42, v42, v196
	v_mul_f32_e32 v43, v43, v196
	v_mul_f32_e32 v44, v44, v196
	v_mul_f32_e32 v45, v45, v196
	v_mul_f32_e32 v46, v46, v196
	v_mul_f32_e32 v47, v47, v196
	v_mul_f32_e32 v32, v148, v32
	v_mul_f32_e32 v33, v149, v33
	v_mul_f32_e32 v34, v150, v34
	v_mul_f32_e32 v35, v151, v35
	v_mul_f32_e32 v36, v152, v36
	v_mul_f32_e32 v37, v153, v37
	v_mul_f32_e32 v38, v154, v38
	v_mul_f32_e32 v39, v155, v39
	v_mul_f32_e32 v40, v156, v40
	v_mul_f32_e32 v41, v157, v41
	v_mul_f32_e32 v42, v158, v42
	v_mul_f32_e32 v43, v159, v43
	v_mul_f32_e32 v44, v160, v44
	v_mul_f32_e32 v45, v161, v45
	v_mul_f32_e32 v46, v162, v46
	v_mul_f32_e32 v47, v163, v47
	v_cvt_pk_bf16_f32 v32, v32, v33
	v_cvt_pk_bf16_f32 v33, v34, v35
	v_cvt_pk_bf16_f32 v34, v36, v37
	v_cvt_pk_bf16_f32 v35, v38, v39
	global_store_dwordx4 v114, v[32:35], s[26:27]
	v_cvt_pk_bf16_f32 v40, v40, v41
	v_cvt_pk_bf16_f32 v41, v42, v43
	v_cvt_pk_bf16_f32 v42, v44, v45
	v_cvt_pk_bf16_f32 v43, v46, v47
	global_store_dwordx4 v114, v[40:43], s[26:27] offset:64
	s_add_u32 s26, s26, 0x12000
	s_addc_u32 s27, s27, 0
	v_mul_f32_e32 v132, v16, v16
	v_mul_f32_e32 v133, v17, v17
	v_mul_f32_e32 v134, v24, v24
	v_mul_f32_e32 v135, v25, v25
	v_fma_f32 v132, v18, v18, v132
	v_fma_f32 v133, v19, v19, v133
	v_fma_f32 v134, v26, v26, v134
	v_fma_f32 v135, v27, v27, v135
	v_fma_f32 v132, v20, v20, v132
	v_fma_f32 v133, v21, v21, v133
	v_fma_f32 v134, v28, v28, v134
	v_fma_f32 v135, v29, v29, v135
	v_fma_f32 v132, v22, v22, v132
	v_fma_f32 v133, v23, v23, v133
	v_fma_f32 v134, v30, v30, v134
	v_fma_f32 v135, v31, v31, v135
	v_add_f32_e32 v132, v132, v134
	v_add_f32_e32 v133, v133, v135
	s_nop 0
	v_add_f32_e32 v194, v132, v133
	ds_swizzle_b32 v195, v194 offset:swizzle(SWAP,16)
	s_waitcnt lgkmcnt(0)
	v_add_f32_e32 v194, v194, v195
	v_mov_b32_e32 v195, v194
	s_nop 1
	v_permlane32_swap_b32_e32 v194, v195
	v_add_f32_e32 v194, v194, v195
	v_fmamk_f32 v194, v194, 0x3c800000, v192
	v_rsq_f32_e32 v194, v194
	s_nop 0
	v_mul_f32_e32 v196, v146, v194
	v_mul_f32_e32 v16, v16, v196
	v_mul_f32_e32 v17, v17, v196
	v_mul_f32_e32 v18, v18, v196
	v_mul_f32_e32 v19, v19, v196
	v_mul_f32_e32 v20, v20, v196
	v_mul_f32_e32 v21, v21, v196
	v_mul_f32_e32 v22, v22, v196
	v_mul_f32_e32 v23, v23, v196
	v_mul_f32_e32 v24, v24, v196
	v_mul_f32_e32 v25, v25, v196
	v_mul_f32_e32 v26, v26, v196
	v_mul_f32_e32 v27, v27, v196
	v_mul_f32_e32 v28, v28, v196
	v_mul_f32_e32 v29, v29, v196
	v_mul_f32_e32 v30, v30, v196
	v_mul_f32_e32 v31, v31, v196
	v_mul_f32_e32 v16, v148, v16
	v_mul_f32_e32 v17, v149, v17
	v_mul_f32_e32 v18, v150, v18
	v_mul_f32_e32 v19, v151, v19
	v_mul_f32_e32 v20, v152, v20
	v_mul_f32_e32 v21, v153, v21
	v_mul_f32_e32 v22, v154, v22
	v_mul_f32_e32 v23, v155, v23
	v_mul_f32_e32 v24, v156, v24
	v_mul_f32_e32 v25, v157, v25
	v_mul_f32_e32 v26, v158, v26
	v_mul_f32_e32 v27, v159, v27
	v_mul_f32_e32 v28, v160, v28
	v_mul_f32_e32 v29, v161, v29
	v_mul_f32_e32 v30, v162, v30
	v_mul_f32_e32 v31, v163, v31
	v_cvt_pk_bf16_f32 v16, v16, v17
	v_cvt_pk_bf16_f32 v17, v18, v19
	v_cvt_pk_bf16_f32 v18, v20, v21
	v_cvt_pk_bf16_f32 v19, v22, v23
	global_store_dwordx4 v114, v[16:19], s[26:27]
	v_cvt_pk_bf16_f32 v24, v24, v25
	v_cvt_pk_bf16_f32 v25, v26, v27
	v_cvt_pk_bf16_f32 v26, v28, v29
	v_cvt_pk_bf16_f32 v27, v30, v31
	global_store_dwordx4 v114, v[24:27], s[26:27] offset:64
	s_add_u32 s26, s26, 0x12000
	s_addc_u32 s27, s27, 0
	v_mul_f32_e32 v132, v0, v0
	v_mul_f32_e32 v133, v1, v1
	v_mul_f32_e32 v134, v8, v8
	v_mul_f32_e32 v135, v9, v9
	v_fma_f32 v132, v2, v2, v132
	v_fma_f32 v133, v3, v3, v133
	v_fma_f32 v134, v10, v10, v134
	v_fma_f32 v135, v11, v11, v135
	v_fma_f32 v132, v4, v4, v132
	v_fma_f32 v133, v5, v5, v133
	v_fma_f32 v134, v12, v12, v134
	v_fma_f32 v135, v13, v13, v135
	v_fma_f32 v132, v6, v6, v132
	v_fma_f32 v133, v7, v7, v133
	v_fma_f32 v134, v14, v14, v134
	v_fma_f32 v135, v15, v15, v135
	v_add_f32_e32 v132, v132, v134
	v_add_f32_e32 v133, v133, v135
	s_nop 0
	v_add_f32_e32 v194, v132, v133
	ds_swizzle_b32 v195, v194 offset:swizzle(SWAP,16)
	s_waitcnt lgkmcnt(0)
	v_add_f32_e32 v194, v194, v195
	v_mov_b32_e32 v195, v194
	s_nop 1
	v_permlane32_swap_b32_e32 v194, v195
	v_add_f32_e32 v194, v194, v195
	v_fmamk_f32 v194, v194, 0x3c800000, v192
	v_rsq_f32_e32 v194, v194
	s_nop 0
	v_mul_f32_e32 v196, v146, v194
	v_mul_f32_e32 v0, v0, v196
	v_mul_f32_e32 v1, v1, v196
	v_mul_f32_e32 v2, v2, v196
	v_mul_f32_e32 v3, v3, v196
	v_mul_f32_e32 v4, v4, v196
	v_mul_f32_e32 v5, v5, v196
	v_mul_f32_e32 v6, v6, v196
	v_mul_f32_e32 v7, v7, v196
	v_mul_f32_e32 v8, v8, v196
	v_mul_f32_e32 v9, v9, v196
	v_mul_f32_e32 v10, v10, v196
	v_mul_f32_e32 v11, v11, v196
	v_mul_f32_e32 v12, v12, v196
	v_mul_f32_e32 v13, v13, v196
	v_mul_f32_e32 v14, v14, v196
	v_mul_f32_e32 v15, v15, v196
	v_mul_f32_e32 v0, v148, v0
	v_mul_f32_e32 v1, v149, v1
	v_mul_f32_e32 v2, v150, v2
	v_mul_f32_e32 v3, v151, v3
	v_mul_f32_e32 v4, v152, v4
	v_mul_f32_e32 v5, v153, v5
	v_mul_f32_e32 v6, v154, v6
	v_mul_f32_e32 v7, v155, v7
	v_mul_f32_e32 v8, v156, v8
	v_mul_f32_e32 v9, v157, v9
	v_mul_f32_e32 v10, v158, v10
	v_mul_f32_e32 v11, v159, v11
	v_mul_f32_e32 v12, v160, v12
	v_mul_f32_e32 v13, v161, v13
	v_mul_f32_e32 v14, v162, v14
	v_mul_f32_e32 v15, v163, v15
	v_cvt_pk_bf16_f32 v0, v0, v1
	v_cvt_pk_bf16_f32 v1, v2, v3
	v_cvt_pk_bf16_f32 v2, v4, v5
	v_cvt_pk_bf16_f32 v3, v6, v7
	global_store_dwordx4 v114, v[0:3], s[26:27]
	v_cvt_pk_bf16_f32 v8, v8, v9
	v_cvt_pk_bf16_f32 v9, v10, v11
	v_cvt_pk_bf16_f32 v10, v12, v13
	v_cvt_pk_bf16_f32 v11, v14, v15
	global_store_dwordx4 v114, v[8:11], s[26:27] offset:64
	s_branch .Lqkv_epi_done

.LBB0_1117:
	s_lshl_b32 s22, s15, 8
	s_lshl_b32 s15, s15, 12
	s_lshl_b32 s17, s17, 8
	s_add_i32 s17, s17, s15
	v_readlane_b32 s72, v253, 34
	s_and_b64 s[2:3], s[2:3], exec
	v_readlane_b32 s73, v253, 35
	v_readlane_b32 s76, v253, 38
	v_readlane_b32 s77, v253, 39
	s_cselect_b32 s2, s17, s22
	s_mov_b64 s[64:65], s[72:73]
	s_mov_b64 s[68:69], s[76:77]
	s_cselect_b32 s15, s65, s69
	s_cselect_b32 s17, s64, s68
	s_ashr_i32 s3, s2, 31
	s_lshl_b64 s[2:3], s[2:3], 12
	v_or_b32_e32 v150, s54, v150
	s_add_u32 s2, s17, s2
	v_ashrrev_i32_e32 v151, 31, v150
	s_addc_u32 s3, s15, s3
	v_lshlrev_b64 v[150:151], 12, v[150:151]
	v_lshl_add_u64 v[150:151], s[2:3], 0, v[150:151]
	v_lshl_add_u64 v[190:191], v[148:149], 2, v[150:151]
	s_mov_b32 s15, 0x10000
	global_load_dwordx4 v[194:197], v[190:191], off offset:16
	global_load_dwordx4 v[198:201], v[190:191], off
	global_load_dwordx4 v[206:209], v[190:191], off offset:528
	global_load_dwordx4 v[210:213], v[190:191], off offset:512
	v_add_co_u32_e32 v150, vcc, s15, v190
	s_mov_b64 s[2:3], 0x10000
	s_nop 0
	v_addc_co_u32_e32 v151, vcc, 0, v191, vcc
	v_lshl_add_u64 v[148:149], v[190:191], 0, s[2:3]
	global_load_dwordx4 v[214:217], v[150:151], off
	global_load_dwordx4 v[218:221], v[148:149], off offset:16
	s_mov_b64 s[2:3], 0x10200
	v_lshl_add_u64 v[148:149], v[190:191], 0, s[2:3]
	s_mov_b64 s[2:3], 0x20000
	global_load_dwordx4 v[184:187], v[150:151], off offset:512
	global_load_dwordx4 v[180:183], v[148:149], off offset:16
	v_lshl_add_u64 v[148:149], v[190:191], 0, s[2:3]
	s_mov_b32 s2, 0x20000
	v_add_co_u32_e32 v150, vcc, s2, v190
	s_mov_b64 s[2:3], 0x20200
	s_nop 0
	v_addc_co_u32_e32 v151, vcc, 0, v191, vcc
	global_load_dwordx4 v[176:179], v[150:151], off
	global_load_dwordx4 v[172:175], v[148:149], off offset:16
	v_lshl_add_u64 v[148:149], v[190:191], 0, s[2:3]
	s_mov_b64 s[2:3], 0x30000
	global_load_dwordx4 v[168:171], v[150:151], off offset:512
	global_load_dwordx4 v[164:167], v[148:149], off offset:16
	v_lshl_add_u64 v[148:149], v[190:191], 0, s[2:3]
	s_mov_b32 s2, 0x30000
	v_add_co_u32_e32 v150, vcc, s2, v190
	s_mov_b64 s[2:3], 0x30200
	s_nop 0
	v_addc_co_u32_e32 v151, vcc, 0, v191, vcc
	global_load_dwordx4 v[160:163], v[150:151], off
	global_load_dwordx4 v[156:159], v[148:149], off offset:16
	v_lshl_add_u64 v[148:149], v[190:191], 0, s[2:3]
	global_load_dwordx4 v[152:155], v[150:151], off offset:512
	s_nop 0
	global_load_dwordx4 v[148:151], v[148:149], off offset:16
	s_mov_b32 s2, 0x8000
	v_readlane_b32 s74, v253, 36
	v_readlane_b32 s75, v253, 37
	v_readlane_b32 s78, v253, 40
	v_readlane_b32 s79, v253, 41
	v_readlane_b32 s80, v253, 42
	v_readlane_b32 s81, v253, 43
	v_readlane_b32 s82, v253, 44
	v_readlane_b32 s83, v253, 45
	v_readlane_b32 s84, v253, 46
	v_readlane_b32 s85, v253, 47
	v_readlane_b32 s86, v253, 48
	v_readlane_b32 s87, v253, 49
	s_waitcnt vmcnt(0) lgkmcnt(0)
	v_fma_f32 v222, v146, v42, v196
	v_fma_f32 v223, v147, v43, v197
	v_fma_f32 v200, v142, v46, v200
	v_fma_f32 v201, v143, v47, v201
	v_fma_f32 v198, v140, v44, v198
	v_fma_f32 v199, v141, v45, v199
	v_fma_f32 v196, v144, v40, v194
	v_fma_f32 v197, v145, v41, v195
	v_cvt_pk_bf16_f32 v194, v198, v199
	v_cvt_pk_bf16_f32 v195, v200, v201
	v_cvt_pk_bf16_f32 v196, v196, v197
	v_cvt_pk_bf16_f32 v197, v222, v223
	flat_store_dwordx4 v[188:189], v[194:197]
	v_fma_f32 v198, v134, v30, v208
	v_fma_f32 v199, v135, v31, v209
	v_fma_f32 v200, v132, v28, v206
	v_fma_f32 v201, v133, v29, v207
	v_fma_f32 v196, v138, v38, v212
	v_fma_f32 v197, v139, v39, v213
	v_fma_f32 v194, v136, v36, v210
	v_fma_f32 v195, v137, v37, v211
	v_fma_f32 v186, v122, v38, v186
	v_fma_f32 v187, v123, v39, v187
	v_cvt_pk_bf16_f32 v194, v194, v195
	v_cvt_pk_bf16_f32 v195, v196, v197
	v_cvt_pk_bf16_f32 v196, v200, v201
	v_cvt_pk_bf16_f32 v197, v198, v199
	flat_store_dwordx4 v[188:189], v[194:197] offset:256
	v_fma_f32 v198, v130, v42, v220
	v_fma_f32 v199, v131, v43, v221
	v_fma_f32 v200, v128, v40, v218
	v_fma_f32 v201, v129, v41, v219
	v_fma_f32 v196, v126, v46, v216
	v_fma_f32 v197, v127, v47, v217
	v_fma_f32 v194, v124, v44, v214
	v_fma_f32 v195, v125, v45, v215
	v_fma_f32 v184, v120, v36, v184
	v_fma_f32 v185, v121, v37, v185
	v_cvt_pk_bf16_f32 v194, v194, v195
	v_cvt_pk_bf16_f32 v195, v196, v197
	v_cvt_pk_bf16_f32 v197, v198, v199
	v_add_co_u32_e32 v198, vcc, s2, v188
	v_cvt_pk_bf16_f32 v196, v200, v201
	s_nop 0
	v_addc_co_u32_e32 v199, vcc, 0, v189, vcc
	flat_store_dwordx4 v[198:199], v[194:197]
	v_fma_f32 v176, v98, v44, v176
	v_fma_f32 v177, v99, v45, v177
	v_fma_f32 v178, v100, v46, v178
	v_fma_f32 v179, v101, v47, v179
	v_fma_f32 v194, v118, v30, v182
	v_fma_f32 v195, v119, v31, v183
	v_fma_f32 v182, v116, v28, v180
	v_fma_f32 v183, v117, v29, v181
	v_cvt_pk_bf16_f32 v180, v184, v185
	v_cvt_pk_bf16_f32 v181, v186, v187
	v_cvt_pk_bf16_f32 v182, v182, v183
	v_cvt_pk_bf16_f32 v183, v194, v195
	flat_store_dwordx4 v[198:199], v[180:183] offset:256
	v_fma_f32 v170, v108, v38, v170
	v_fma_f32 v171, v109, v39, v171
	v_fma_f32 v168, v106, v36, v168
	v_fma_f32 v169, v107, v37, v169
	v_fma_f32 v180, v104, v42, v174
	v_fma_f32 v181, v105, v43, v175
	v_fma_f32 v174, v102, v40, v172
	v_fma_f32 v175, v103, v41, v173
	v_cvt_pk_bf16_f32 v172, v176, v177
	v_add_co_u32_e32 v176, vcc, s15, v188
	v_cvt_pk_bf16_f32 v173, v178, v179
	v_cvt_pk_bf16_f32 v174, v174, v175
	v_cvt_pk_bf16_f32 v175, v180, v181
	v_addc_co_u32_e32 v177, vcc, 0, v189, vcc
	flat_store_dwordx4 v[176:177], v[172:175]
	v_fma_f32 v160, v82, v44, v160
	v_fma_f32 v161, v83, v45, v161
	s_mov_b32 s2, 0x18000
	v_fma_f32 v172, v112, v30, v166
	v_fma_f32 v173, v113, v31, v167
	v_fma_f32 v166, v110, v28, v164
	v_fma_f32 v167, v111, v29, v165
	v_cvt_pk_bf16_f32 v164, v168, v169
	v_cvt_pk_bf16_f32 v165, v170, v171
	v_cvt_pk_bf16_f32 v166, v166, v167
	v_cvt_pk_bf16_f32 v167, v172, v173
	flat_store_dwordx4 v[176:177], v[164:167] offset:256
	v_fma_f32 v162, v84, v46, v162
	v_fma_f32 v163, v85, v47, v163
	v_fma_f32 v152, v90, v36, v152
	v_fma_f32 v153, v91, v37, v153
	v_fma_f32 v164, v88, v42, v158
	v_fma_f32 v165, v89, v43, v159
	v_fma_f32 v158, v86, v40, v156
	v_fma_f32 v159, v87, v41, v157
	v_cvt_pk_bf16_f32 v156, v160, v161
	v_add_co_u32_e32 v160, vcc, s2, v188
	v_cvt_pk_bf16_f32 v157, v162, v163
	v_cvt_pk_bf16_f32 v158, v158, v159
	v_cvt_pk_bf16_f32 v159, v164, v165
	v_addc_co_u32_e32 v161, vcc, 0, v189, vcc
	s_mov_b64 s[2:3], 0x80000
	flat_store_dwordx4 v[160:161], v[156:159]
	v_fma_f32 v154, v92, v38, v154
	v_fma_f32 v155, v93, v39, v155
	s_nop 0
	v_fma_f32 v156, v96, v30, v150
	v_fma_f32 v157, v97, v31, v151
	v_fma_f32 v150, v94, v28, v148
	v_fma_f32 v151, v95, v29, v149
	v_cvt_pk_bf16_f32 v148, v152, v153
	v_lshl_add_u64 v[152:153], v[190:191], 0, s[2:3]
	s_mov_b32 s2, 0x80000
	v_cvt_pk_bf16_f32 v149, v154, v155
	v_cvt_pk_bf16_f32 v150, v150, v151
	v_cvt_pk_bf16_f32 v151, v156, v157
	v_add_co_u32_e32 v156, vcc, s2, v190
	flat_store_dwordx4 v[160:161], v[148:151] offset:256
	s_nop 0
	v_addc_co_u32_e32 v157, vcc, 0, v191, vcc
	global_load_dwordx4 v[148:151], v[156:157], off
	s_nop 0
	global_load_dwordx4 v[152:155], v[152:153], off offset:16
	s_mov_b64 s[2:3], 0x80200
	v_lshl_add_u64 v[160:161], v[190:191], 0, s[2:3]
	s_mov_b64 s[2:3], 0x90000
	v_lshl_add_u64 v[168:169], v[190:191], 0, s[2:3]
	s_mov_b32 s2, 0x90000
	global_load_dwordx4 v[156:159], v[156:157], off offset:512
	s_nop 0
	global_load_dwordx4 v[160:163], v[160:161], off offset:16
	v_add_co_u32_e32 v172, vcc, s2, v190
	s_mov_b64 s[2:3], 0x90200
	s_nop 0
	v_addc_co_u32_e32 v173, vcc, 0, v191, vcc
	global_load_dwordx4 v[164:167], v[172:173], off
	s_nop 0
	global_load_dwordx4 v[168:171], v[168:169], off offset:16
	v_lshl_add_u64 v[176:177], v[190:191], 0, s[2:3]
	s_mov_b64 s[2:3], 0xa0000
	v_lshl_add_u64 v[184:185], v[190:191], 0, s[2:3]
	s_mov_b32 s2, 0xa0000
	global_load_dwordx4 v[172:175], v[172:173], off offset:512
	s_nop 0
	global_load_dwordx4 v[176:179], v[176:177], off offset:16
	v_add_co_u32_e32 v194, vcc, s2, v190
	s_mov_b64 s[2:3], 0xa0200
	s_nop 0
	v_addc_co_u32_e32 v195, vcc, 0, v191, vcc
	global_load_dwordx4 v[180:183], v[194:195], off
	s_nop 0
	global_load_dwordx4 v[184:187], v[184:185], off offset:16
	v_lshl_add_u64 v[198:199], v[190:191], 0, s[2:3]
	s_mov_b64 s[2:3], 0xb0000
	v_lshl_add_u64 v[210:211], v[190:191], 0, s[2:3]
	s_mov_b32 s2, 0xb0000
	global_load_dwordx4 v[194:197], v[194:195], off offset:512
	s_nop 0
	global_load_dwordx4 v[198:201], v[198:199], off offset:16
	v_add_co_u32_e32 v214, vcc, s2, v190
	s_mov_b64 s[2:3], 0xb0200
	s_nop 0
	v_addc_co_u32_e32 v215, vcc, 0, v191, vcc
	global_load_dwordx4 v[206:209], v[214:215], off
	s_nop 0
	global_load_dwordx4 v[210:213], v[210:211], off offset:16
	v_lshl_add_u64 v[190:191], v[190:191], 0, s[2:3]
	global_load_dwordx4 v[214:217], v[214:215], off offset:512
	s_nop 0
	global_load_dwordx4 v[218:221], v[190:191], off offset:16
	s_mov_b32 s2, 0x40000
	s_waitcnt vmcnt(0)
	v_fma_f32 v150, v80, v46, v150
	v_fma_f32 v151, v81, v47, v151
	v_fma_f32 v148, v78, v44, v148
	v_fma_f32 v149, v79, v45, v149
	v_fma_f32 v152, v74, v40, v152
	v_fma_f32 v153, v75, v41, v153
	v_fma_f32 v154, v76, v42, v154
	v_fma_f32 v155, v77, v43, v155
	v_cvt_pk_bf16_f32 v148, v148, v149
	v_cvt_pk_bf16_f32 v149, v150, v151
	v_cvt_pk_bf16_f32 v150, v152, v153
	v_add_co_u32_e32 v152, vcc, s2, v188
	v_cvt_pk_bf16_f32 v151, v154, v155
	s_nop 0
	v_addc_co_u32_e32 v153, vcc, 0, v189, vcc
	flat_store_dwordx4 v[152:153], v[148:151]
	v_fma_f32 v154, v68, v30, v162
	v_fma_f32 v155, v69, v31, v163
	s_mov_b32 s2, 0x48000
	v_fma_f32 v150, v72, v38, v158
	v_fma_f32 v151, v73, v39, v159
	v_fma_f32 v148, v70, v36, v156
	v_fma_f32 v149, v71, v37, v157
	v_fma_f32 v156, v66, v28, v160
	v_fma_f32 v157, v67, v29, v161
	v_cvt_pk_bf16_f32 v148, v148, v149
	v_cvt_pk_bf16_f32 v149, v150, v151
	v_cvt_pk_bf16_f32 v150, v156, v157
	v_cvt_pk_bf16_f32 v151, v154, v155
	flat_store_dwordx4 v[152:153], v[148:151] offset:256
	v_fma_f32 v152, v58, v42, v170
	v_fma_f32 v153, v59, v43, v171
	v_fma_f32 v154, v56, v40, v168
	v_fma_f32 v155, v57, v41, v169
	v_fma_f32 v150, v62, v46, v166
	v_fma_f32 v151, v63, v47, v167
	v_fma_f32 v148, v60, v44, v164
	v_fma_f32 v149, v61, v45, v165
	v_fma_f32 v156, v48, v28, v176
	v_fma_f32 v157, v49, v29, v177
	v_cvt_pk_bf16_f32 v148, v148, v149
	v_cvt_pk_bf16_f32 v149, v150, v151
	v_cvt_pk_bf16_f32 v151, v152, v153
	v_add_co_u32_e32 v152, vcc, s2, v188
	v_cvt_pk_bf16_f32 v150, v154, v155
	s_nop 0
	v_addc_co_u32_e32 v153, vcc, 0, v189, vcc
	flat_store_dwordx4 v[152:153], v[148:151]
	v_fma_f32 v154, v50, v30, v178
	v_fma_f32 v155, v51, v31, v179
	s_mov_b32 s2, 0x50000
	v_fma_f32 v150, v54, v38, v174
	v_fma_f32 v151, v55, v39, v175
	v_fma_f32 v148, v52, v36, v172
	v_fma_f32 v149, v53, v37, v173
	s_nop 0
	v_cvt_pk_bf16_f32 v148, v148, v149
	v_cvt_pk_bf16_f32 v149, v150, v151
	v_cvt_pk_bf16_f32 v150, v156, v157
	v_cvt_pk_bf16_f32 v151, v154, v155
	flat_store_dwordx4 v[152:153], v[148:151] offset:256
	v_fma_f32 v152, v26, v42, v186
	v_fma_f32 v153, v27, v43, v187
	v_fma_f32 v154, v24, v40, v184
	v_fma_f32 v155, v25, v41, v185
	v_fma_f32 v150, v34, v46, v182
	v_fma_f32 v151, v35, v47, v183
	v_fma_f32 v148, v32, v44, v180
	v_fma_f32 v149, v33, v45, v181
	v_fma_f32 v156, v16, v28, v198
	v_fma_f32 v157, v17, v29, v199
	v_cvt_pk_bf16_f32 v148, v148, v149
	v_cvt_pk_bf16_f32 v149, v150, v151
	v_cvt_pk_bf16_f32 v151, v152, v153
	v_add_co_u32_e32 v152, vcc, s2, v188
	v_cvt_pk_bf16_f32 v150, v154, v155
	s_nop 0
	v_addc_co_u32_e32 v153, vcc, 0, v189, vcc
	flat_store_dwordx4 v[152:153], v[148:151]
	v_fma_f32 v154, v18, v30, v200
	v_fma_f32 v155, v19, v31, v201
	s_mov_b32 s2, 0x58000
	v_fma_f32 v150, v22, v38, v196
	v_fma_f32 v151, v23, v39, v197
	v_fma_f32 v148, v20, v36, v194
	v_fma_f32 v149, v21, v37, v195
	s_nop 0
	v_cvt_pk_bf16_f32 v148, v148, v149
	v_cvt_pk_bf16_f32 v149, v150, v151
	v_cvt_pk_bf16_f32 v150, v156, v157
	v_cvt_pk_bf16_f32 v151, v154, v155
	flat_store_dwordx4 v[152:153], v[148:151] offset:256
	v_fma_f32 v152, v10, v42, v212
	v_fma_f32 v153, v11, v43, v213
	v_fma_f32 v154, v8, v40, v210
	v_fma_f32 v155, v9, v41, v211
	v_fma_f32 v150, v14, v46, v208
	v_fma_f32 v151, v15, v47, v209
	v_fma_f32 v148, v12, v44, v206
	v_fma_f32 v149, v13, v45, v207
	v_fma_f32 v156, v0, v28, v218
	v_fma_f32 v157, v1, v29, v219
	v_cvt_pk_bf16_f32 v148, v148, v149
	v_cvt_pk_bf16_f32 v149, v150, v151
	v_cvt_pk_bf16_f32 v151, v152, v153
	v_add_co_u32_e32 v152, vcc, s2, v188
	v_cvt_pk_bf16_f32 v150, v154, v155
	s_nop 0
	v_addc_co_u32_e32 v153, vcc, 0, v189, vcc
	flat_store_dwordx4 v[152:153], v[148:151]
	v_fma_f32 v154, v2, v30, v220
	v_fma_f32 v155, v3, v31, v221
	s_nop 0
	v_fma_f32 v150, v6, v38, v216
	v_fma_f32 v151, v7, v39, v217
	v_fma_f32 v148, v4, v36, v214
	v_fma_f32 v149, v5, v37, v215
	s_nop 0
	v_cvt_pk_bf16_f32 v148, v148, v149
	v_cvt_pk_bf16_f32 v149, v150, v151
	v_cvt_pk_bf16_f32 v150, v156, v157
	v_cvt_pk_bf16_f32 v151, v154, v155
	flat_store_dwordx4 v[152:153], v[148:151] offset:256
	s_cbranch_execnz .LBB0_1116
.LBB0_1118:
	s_mov_b32 s2, 0x40000
	s_nop 0
	global_load_dwordx4 v[174:177], v[188:189], off
	global_load_dwordx4 v[178:181], v[188:189], off offset:256
	v_add_co_u32_e32 v172, vcc, 0x8000, v188
	s_nop 0
	v_addc_co_u32_e32 v173, vcc, 0, v189, vcc
	global_load_dwordx4 v[182:185], v[172:173], off
	global_load_dwordx4 v[164:167], v[172:173], off offset:256
	v_add_co_u32_e32 v170, vcc, 0x10000, v188
	s_nop 0
	v_addc_co_u32_e32 v171, vcc, 0, v189, vcc
	global_load_dwordx4 v[160:163], v[170:171], off
	global_load_dwordx4 v[152:155], v[170:171], off offset:256
	v_add_co_u32_e32 v168, vcc, 0x18000, v188
	s_nop 0
	v_addc_co_u32_e32 v169, vcc, 0, v189, vcc
	global_load_dwordx4 v[156:159], v[168:169], off
	global_load_dwordx4 v[148:151], v[168:169], off offset:256
	v_add_co_u32_e32 v198, vcc, 0x40000, v188
	s_nop 0
	v_addc_co_u32_e32 v199, vcc, 0, v189, vcc
	global_load_dwordx4 v[194:197], v[198:199], off
	global_load_dwordx4 v[198:201], v[198:199], off offset:256
	v_add_co_u32_e32 v210, vcc, 0x48000, v188
	s_nop 0
	v_addc_co_u32_e32 v211, vcc, 0, v189, vcc
	global_load_dwordx4 v[206:209], v[210:211], off
	global_load_dwordx4 v[210:213], v[210:211], off offset:256
	v_add_co_u32_e32 v218, vcc, 0x50000, v188
	s_nop 0
	v_addc_co_u32_e32 v219, vcc, 0, v189, vcc
	global_load_dwordx4 v[214:217], v[218:219], off
	global_load_dwordx4 v[218:221], v[218:219], off offset:256
	v_add_co_u32_e32 v226, vcc, 0x58000, v188
	s_nop 0
	v_addc_co_u32_e32 v227, vcc, 0, v189, vcc
	global_load_dwordx4 v[222:225], v[226:227], off
	global_load_dwordx4 v[226:229], v[226:227], off offset:256
	s_waitcnt vmcnt(12) lgkmcnt(0)
	v_lshlrev_b32_e32 v186, 16, v174
	v_and_b32_e32 v187, 0xffff0000, v174
	s_nop 0
	v_lshlrev_b32_e32 v174, 16, v175
	v_and_b32_e32 v175, 0xffff0000, v175
	v_lshlrev_b32_e32 v190, 16, v176
	v_and_b32_e32 v191, 0xffff0000, v176
	v_lshlrev_b32_e32 v176, 16, v177
	v_and_b32_e32 v177, 0xffff0000, v177
	v_fma_f32 v142, v142, v46, v174
	v_fma_f32 v143, v143, v47, v175
	v_fma_f32 v140, v140, v44, v186
	v_fma_f32 v141, v141, v45, v187
	v_fma_f32 v146, v146, v42, v176
	v_fma_f32 v147, v147, v43, v177
	v_fma_f32 v144, v144, v40, v190
	v_fma_f32 v145, v145, v41, v191
	v_cvt_pk_bf16_f32 v140, v140, v141
	v_cvt_pk_bf16_f32 v141, v142, v143
	v_cvt_pk_bf16_f32 v142, v144, v145
	v_cvt_pk_bf16_f32 v143, v146, v147
	global_store_dwordx4 v[188:189], v[140:143], off
	v_lshlrev_b32_e32 v144, 16, v180
	v_and_b32_e32 v145, 0xffff0000, v180
	v_lshlrev_b32_e32 v140, 16, v178
	v_and_b32_e32 v141, 0xffff0000, v178
	v_lshlrev_b32_e32 v142, 16, v179
	v_and_b32_e32 v143, 0xffff0000, v179
	v_lshlrev_b32_e32 v146, 16, v181
	v_and_b32_e32 v147, 0xffff0000, v181
	v_fma_f32 v138, v138, v38, v142
	v_fma_f32 v139, v139, v39, v143
	v_fma_f32 v136, v136, v36, v140
	v_fma_f32 v137, v137, v37, v141
	v_fma_f32 v140, v134, v30, v146
	v_fma_f32 v141, v135, v31, v147
	v_fma_f32 v134, v132, v28, v144
	v_fma_f32 v135, v133, v29, v145
	v_cvt_pk_bf16_f32 v132, v136, v137
	v_cvt_pk_bf16_f32 v133, v138, v139
	v_cvt_pk_bf16_f32 v134, v134, v135
	v_cvt_pk_bf16_f32 v135, v140, v141
	global_store_dwordx4 v[188:189], v[132:135], off offset:256
	v_lshlrev_b32_e32 v136, 16, v184
	v_and_b32_e32 v137, 0xffff0000, v184
	v_lshlrev_b32_e32 v132, 16, v182
	v_and_b32_e32 v133, 0xffff0000, v182
	v_lshlrev_b32_e32 v134, 16, v183
	v_and_b32_e32 v135, 0xffff0000, v183
	v_lshlrev_b32_e32 v138, 16, v185
	v_and_b32_e32 v139, 0xffff0000, v185
	v_fma_f32 v126, v126, v46, v134
	v_fma_f32 v127, v127, v47, v135
	v_fma_f32 v124, v124, v44, v132
	v_fma_f32 v125, v125, v45, v133
	v_fma_f32 v130, v130, v42, v138
	v_fma_f32 v131, v131, v43, v139
	v_fma_f32 v128, v128, v40, v136
	v_fma_f32 v129, v129, v41, v137
	v_cvt_pk_bf16_f32 v124, v124, v125
	v_cvt_pk_bf16_f32 v125, v126, v127
	v_cvt_pk_bf16_f32 v126, v128, v129
	v_cvt_pk_bf16_f32 v127, v130, v131
	global_store_dwordx4 v[172:173], v[124:127], off
	v_lshlrev_b32_e32 v128, 16, v166
	v_and_b32_e32 v129, 0xffff0000, v166
	v_lshlrev_b32_e32 v124, 16, v164
	v_and_b32_e32 v125, 0xffff0000, v164
	v_lshlrev_b32_e32 v126, 16, v165
	v_and_b32_e32 v127, 0xffff0000, v165
	v_lshlrev_b32_e32 v130, 16, v167
	v_and_b32_e32 v131, 0xffff0000, v167
	v_fma_f32 v122, v122, v38, v126
	v_fma_f32 v123, v123, v39, v127
	v_fma_f32 v120, v120, v36, v124
	v_fma_f32 v121, v121, v37, v125
	v_fma_f32 v124, v118, v30, v130
	v_fma_f32 v125, v119, v31, v131
	v_fma_f32 v118, v116, v28, v128
	v_fma_f32 v119, v117, v29, v129
	v_cvt_pk_bf16_f32 v116, v120, v121
	v_cvt_pk_bf16_f32 v117, v122, v123
	v_cvt_pk_bf16_f32 v118, v118, v119
	v_cvt_pk_bf16_f32 v119, v124, v125
	global_store_dwordx4 v[172:173], v[116:119], off offset:256
	s_waitcnt vmcnt(12)
	v_lshlrev_b32_e32 v120, 16, v162
	v_lshlrev_b32_e32 v116, 16, v160
	v_and_b32_e32 v117, 0xffff0000, v160
	v_lshlrev_b32_e32 v118, 16, v161
	v_and_b32_e32 v119, 0xffff0000, v161
	v_and_b32_e32 v121, 0xffff0000, v162
	v_lshlrev_b32_e32 v122, 16, v163
	v_and_b32_e32 v123, 0xffff0000, v163
	v_fma_f32 v100, v100, v46, v118
	v_fma_f32 v101, v101, v47, v119
	v_fma_f32 v98, v98, v44, v116
	v_fma_f32 v99, v99, v45, v117
	v_fma_f32 v104, v104, v42, v122
	v_fma_f32 v105, v105, v43, v123
	v_fma_f32 v102, v102, v40, v120
	v_fma_f32 v103, v103, v41, v121
	v_cvt_pk_bf16_f32 v98, v98, v99
	v_cvt_pk_bf16_f32 v99, v100, v101
	v_cvt_pk_bf16_f32 v100, v102, v103
	v_cvt_pk_bf16_f32 v101, v104, v105
	global_store_dwordx4 v[170:171], v[98:101], off
	v_lshlrev_b32_e32 v102, 16, v154
	v_and_b32_e32 v103, 0xffff0000, v154
	v_lshlrev_b32_e32 v98, 16, v152
	v_and_b32_e32 v99, 0xffff0000, v152
	v_lshlrev_b32_e32 v100, 16, v153
	v_and_b32_e32 v101, 0xffff0000, v153
	v_lshlrev_b32_e32 v104, 16, v155
	v_and_b32_e32 v105, 0xffff0000, v155
	v_fma_f32 v100, v108, v38, v100
	v_fma_f32 v101, v109, v39, v101
	v_fma_f32 v98, v106, v36, v98
	v_fma_f32 v99, v107, v37, v99
	v_fma_f32 v104, v112, v30, v104
	v_fma_f32 v105, v113, v31, v105
	v_fma_f32 v102, v110, v28, v102
	v_fma_f32 v103, v111, v29, v103
	v_cvt_pk_bf16_f32 v98, v98, v99
	v_cvt_pk_bf16_f32 v99, v100, v101
	v_cvt_pk_bf16_f32 v100, v102, v103
	v_cvt_pk_bf16_f32 v101, v104, v105
	global_store_dwordx4 v[170:171], v[98:101], off offset:256
	v_lshlrev_b32_e32 v102, 16, v158
	v_and_b32_e32 v103, 0xffff0000, v158
	v_lshlrev_b32_e32 v98, 16, v156
	v_and_b32_e32 v99, 0xffff0000, v156
	v_lshlrev_b32_e32 v100, 16, v157
	v_and_b32_e32 v101, 0xffff0000, v157
	v_lshlrev_b32_e32 v104, 16, v159
	v_and_b32_e32 v105, 0xffff0000, v159
	v_fma_f32 v84, v84, v46, v100
	v_fma_f32 v85, v85, v47, v101
	v_fma_f32 v82, v82, v44, v98
	v_fma_f32 v83, v83, v45, v99
	v_fma_f32 v88, v88, v42, v104
	v_fma_f32 v89, v89, v43, v105
	v_fma_f32 v86, v86, v40, v102
	v_fma_f32 v87, v87, v41, v103
	v_cvt_pk_bf16_f32 v82, v82, v83
	v_cvt_pk_bf16_f32 v83, v84, v85
	v_cvt_pk_bf16_f32 v84, v86, v87
	v_cvt_pk_bf16_f32 v85, v88, v89
	global_store_dwordx4 v[168:169], v[82:85], off
	v_lshlrev_b32_e32 v86, 16, v150
	v_and_b32_e32 v87, 0xffff0000, v150
	v_lshlrev_b32_e32 v82, 16, v148
	v_and_b32_e32 v83, 0xffff0000, v148
	v_lshlrev_b32_e32 v84, 16, v149
	v_and_b32_e32 v85, 0xffff0000, v149
	v_lshlrev_b32_e32 v88, 16, v151
	v_and_b32_e32 v89, 0xffff0000, v151
	v_fma_f32 v84, v92, v38, v84
	v_fma_f32 v85, v93, v39, v85
	v_fma_f32 v82, v90, v36, v82
	v_fma_f32 v83, v91, v37, v83
	v_fma_f32 v88, v96, v30, v88
	v_fma_f32 v89, v97, v31, v89
	v_fma_f32 v86, v94, v28, v86
	v_fma_f32 v87, v95, v29, v87
	v_cvt_pk_bf16_f32 v82, v82, v83
	v_cvt_pk_bf16_f32 v83, v84, v85
	v_cvt_pk_bf16_f32 v84, v86, v87
	v_cvt_pk_bf16_f32 v85, v88, v89
	v_add_co_u32_e32 v86, vcc, s2, v188
	global_store_dwordx4 v[168:169], v[82:85], off offset:256
	s_nop 0
	v_addc_co_u32_e32 v87, vcc, 0, v189, vcc
	s_mov_b32 s2, 0x48000
	v_add_co_u32_e32 v88, vcc, s2, v188
	s_mov_b32 s2, 0x50000
	s_nop 0
	v_addc_co_u32_e32 v89, vcc, 0, v189, vcc
	v_add_co_u32_e32 v112, vcc, s2, v188
	s_mov_b32 s2, 0x58000
	s_nop 0
	v_addc_co_u32_e32 v113, vcc, 0, v189, vcc
	v_add_co_u32_e32 v90, vcc, s2, v188
	s_waitcnt vmcnt(10)
	v_lshlrev_b32_e32 v124, 16, v194
	v_addc_co_u32_e32 v91, vcc, 0, v189, vcc
	v_and_b32_e32 v125, 0xffff0000, v194
	v_lshlrev_b32_e32 v82, 16, v195
	v_and_b32_e32 v83, 0xffff0000, v195
	v_lshlrev_b32_e32 v126, 16, v196
	v_and_b32_e32 v127, 0xffff0000, v196
	v_lshlrev_b32_e32 v84, 16, v197
	v_and_b32_e32 v85, 0xffff0000, v197
	v_fma_f32 v80, v80, v46, v82
	v_fma_f32 v81, v81, v47, v83
	v_fma_f32 v78, v78, v44, v124
	v_fma_f32 v79, v79, v45, v125
	v_fma_f32 v82, v76, v42, v84
	v_fma_f32 v83, v77, v43, v85
	v_fma_f32 v76, v74, v40, v126
	v_fma_f32 v77, v75, v41, v127
	v_cvt_pk_bf16_f32 v74, v78, v79
	v_cvt_pk_bf16_f32 v75, v80, v81
	v_cvt_pk_bf16_f32 v76, v76, v77
	v_cvt_pk_bf16_f32 v77, v82, v83
	global_store_dwordx4 v[86:87], v[74:77], off
	v_lshlrev_b32_e32 v78, 16, v200
	v_and_b32_e32 v79, 0xffff0000, v200
	v_lshlrev_b32_e32 v74, 16, v198
	v_and_b32_e32 v75, 0xffff0000, v198
	v_lshlrev_b32_e32 v76, 16, v199
	v_and_b32_e32 v77, 0xffff0000, v199
	v_lshlrev_b32_e32 v80, 16, v201
	v_and_b32_e32 v81, 0xffff0000, v201
	v_fma_f32 v72, v72, v38, v76
	v_fma_f32 v73, v73, v39, v77
	v_fma_f32 v70, v70, v36, v74
	v_fma_f32 v71, v71, v37, v75
	v_fma_f32 v74, v68, v30, v80
	v_fma_f32 v75, v69, v31, v81
	v_fma_f32 v68, v66, v28, v78
	v_fma_f32 v69, v67, v29, v79
	v_cvt_pk_bf16_f32 v66, v70, v71
	v_cvt_pk_bf16_f32 v67, v72, v73
	v_cvt_pk_bf16_f32 v68, v68, v69
	v_cvt_pk_bf16_f32 v69, v74, v75
	global_store_dwordx4 v[86:87], v[66:69], off offset:256
	v_lshlrev_b32_e32 v70, 16, v208
	v_and_b32_e32 v71, 0xffff0000, v208
	v_lshlrev_b32_e32 v66, 16, v206
	v_and_b32_e32 v67, 0xffff0000, v206
	v_lshlrev_b32_e32 v68, 16, v207
	v_and_b32_e32 v69, 0xffff0000, v207
	v_lshlrev_b32_e32 v72, 16, v209
	v_and_b32_e32 v73, 0xffff0000, v209
	v_fma_f32 v62, v62, v46, v68
	v_fma_f32 v63, v63, v47, v69
	v_fma_f32 v60, v60, v44, v66
	v_fma_f32 v61, v61, v45, v67
	v_fma_f32 v66, v58, v42, v72
	v_fma_f32 v67, v59, v43, v73
	v_fma_f32 v58, v56, v40, v70
	v_fma_f32 v59, v57, v41, v71
	v_cvt_pk_bf16_f32 v56, v60, v61
	v_cvt_pk_bf16_f32 v57, v62, v63
	v_cvt_pk_bf16_f32 v58, v58, v59
	v_cvt_pk_bf16_f32 v59, v66, v67
	global_store_dwordx4 v[88:89], v[56:59], off
	v_lshlrev_b32_e32 v60, 16, v212
	v_and_b32_e32 v61, 0xffff0000, v212
	v_lshlrev_b32_e32 v56, 16, v210
	v_and_b32_e32 v57, 0xffff0000, v210
	v_lshlrev_b32_e32 v58, 16, v211
	v_and_b32_e32 v59, 0xffff0000, v211
	v_lshlrev_b32_e32 v62, 16, v213
	v_and_b32_e32 v63, 0xffff0000, v213
	v_fma_f32 v54, v54, v38, v58
	v_fma_f32 v55, v55, v39, v59
	v_fma_f32 v52, v52, v36, v56
	v_fma_f32 v53, v53, v37, v57
	v_fma_f32 v56, v50, v30, v62
	v_fma_f32 v57, v51, v31, v63
	v_fma_f32 v50, v48, v28, v60
	v_fma_f32 v51, v49, v29, v61
	v_cvt_pk_bf16_f32 v48, v52, v53
	v_cvt_pk_bf16_f32 v49, v54, v55
	v_cvt_pk_bf16_f32 v50, v50, v51
	v_cvt_pk_bf16_f32 v51, v56, v57
	global_store_dwordx4 v[88:89], v[48:51], off offset:256
	v_lshlrev_b32_e32 v52, 16, v216
	v_and_b32_e32 v53, 0xffff0000, v216
	v_lshlrev_b32_e32 v48, 16, v214
	v_and_b32_e32 v49, 0xffff0000, v214
	v_lshlrev_b32_e32 v50, 16, v215
	v_and_b32_e32 v51, 0xffff0000, v215
	v_lshlrev_b32_e32 v54, 16, v217
	v_and_b32_e32 v55, 0xffff0000, v217
	v_fma_f32 v34, v34, v46, v50
	v_fma_f32 v35, v35, v47, v51
	v_fma_f32 v32, v32, v44, v48
	v_fma_f32 v33, v33, v45, v49
	v_fma_f32 v48, v26, v42, v54
	v_fma_f32 v49, v27, v43, v55
	v_fma_f32 v26, v24, v40, v52
	v_fma_f32 v27, v25, v41, v53
	v_cvt_pk_bf16_f32 v24, v32, v33
	v_cvt_pk_bf16_f32 v25, v34, v35
	v_cvt_pk_bf16_f32 v26, v26, v27
	v_cvt_pk_bf16_f32 v27, v48, v49
	global_store_dwordx4 v[112:113], v[24:27], off
	v_lshlrev_b32_e32 v32, 16, v220
	v_and_b32_e32 v33, 0xffff0000, v220
	v_lshlrev_b32_e32 v24, 16, v218
	v_and_b32_e32 v25, 0xffff0000, v218
	v_lshlrev_b32_e32 v26, 16, v219
	v_and_b32_e32 v27, 0xffff0000, v219
	v_lshlrev_b32_e32 v34, 16, v221
	v_and_b32_e32 v35, 0xffff0000, v221
	v_fma_f32 v22, v22, v38, v26
	v_fma_f32 v23, v23, v39, v27
	v_fma_f32 v20, v20, v36, v24
	v_fma_f32 v21, v21, v37, v25
	v_fma_f32 v24, v18, v30, v34
	v_fma_f32 v25, v19, v31, v35
	v_fma_f32 v18, v16, v28, v32
	v_fma_f32 v19, v17, v29, v33
	v_cvt_pk_bf16_f32 v16, v20, v21
	v_cvt_pk_bf16_f32 v17, v22, v23
	v_cvt_pk_bf16_f32 v18, v18, v19
	v_cvt_pk_bf16_f32 v19, v24, v25
	global_store_dwordx4 v[112:113], v[16:19], off offset:256
	s_waitcnt vmcnt(14)
	v_lshlrev_b32_e32 v20, 16, v224
	v_and_b32_e32 v21, 0xffff0000, v224
	v_lshlrev_b32_e32 v16, 16, v222
	v_and_b32_e32 v17, 0xffff0000, v222
	v_lshlrev_b32_e32 v18, 16, v223
	v_and_b32_e32 v19, 0xffff0000, v223
	v_lshlrev_b32_e32 v22, 16, v225
	v_and_b32_e32 v23, 0xffff0000, v225
	v_fma_f32 v14, v14, v46, v18
	v_fma_f32 v15, v15, v47, v19
	v_fma_f32 v12, v12, v44, v16
	v_fma_f32 v13, v13, v45, v17
	v_fma_f32 v16, v10, v42, v22
	v_fma_f32 v17, v11, v43, v23
	v_fma_f32 v10, v8, v40, v20
	v_fma_f32 v11, v9, v41, v21
	v_cvt_pk_bf16_f32 v8, v12, v13
	v_cvt_pk_bf16_f32 v9, v14, v15
	v_cvt_pk_bf16_f32 v10, v10, v11
	v_cvt_pk_bf16_f32 v11, v16, v17
	global_store_dwordx4 v[90:91], v[8:11], off
	v_lshlrev_b32_e32 v12, 16, v228
	v_and_b32_e32 v13, 0xffff0000, v228
	v_lshlrev_b32_e32 v8, 16, v226
	v_and_b32_e32 v9, 0xffff0000, v226
	v_lshlrev_b32_e32 v10, 16, v227
	v_and_b32_e32 v11, 0xffff0000, v227
	v_lshlrev_b32_e32 v14, 16, v229
	v_and_b32_e32 v15, 0xffff0000, v229
	v_fma_f32 v6, v6, v38, v10
	v_fma_f32 v7, v7, v39, v11
	v_fma_f32 v4, v4, v36, v8
	v_fma_f32 v5, v5, v37, v9
	v_fma_f32 v8, v2, v30, v14
	v_fma_f32 v9, v3, v31, v15
	v_fma_f32 v2, v0, v28, v12
	v_fma_f32 v3, v1, v29, v13
	v_cvt_pk_bf16_f32 v0, v4, v5
	v_cvt_pk_bf16_f32 v1, v6, v7
	v_cvt_pk_bf16_f32 v2, v2, v3
	v_cvt_pk_bf16_f32 v3, v8, v9
	global_store_dwordx4 v[90:91], v[0:3], off offset:256
	s_andn2_b64 vcc, exec, s[0:1]
	s_mov_b64 s[0:1], -1
	s_cbranch_vccnz .LBB0_1107

.LBB0_1428:
	s_lshl_b32 s2, s61, 8
	v_mbcnt_lo_u32_b32 v133, -1, 0
	v_mbcnt_hi_u32_b32 v133, -1, v133
	s_add_i32 s2, s2, s49
	v_and_or_b32 v132, v133, 15, s2
	s_lshl_b32 s2, s62, 7
	v_ashrrev_i32_e32 v133, 1, v133
	s_or_b32 s2, s2, s50
	v_and_b32_e32 v133, -8, v133
	v_add_u32_e32 v142, s2, v133
	v_mul_f32_e32 v133, 0xbfb8aa3b, v128
	v_exp_f32_e32 v133, v133
	v_mul_f32_e32 v143, 0xbfb8aa3b, v129
	v_exp_f32_e32 v145, v143
	v_ashrrev_i32_e32 v143, 31, v142
	v_add_f32_e32 v133, 1.0, v133
	v_rcp_f32_e32 v144, v133
	v_add_f32_e32 v133, 1.0, v145
	v_rcp_f32_e32 v145, v133
	v_ashrrev_i32_e32 v133, 31, v132
	v_lshlrev_b64 v[146:147], 11, v[132:133]
	v_mul_f32_e32 v133, 0xbfb8aa3b, v130
	v_mul_f32_e32 v128, v128, v144
	v_mul_f32_e32 v129, v129, v145
	v_mul_f32_e32 v144, 0xbfb8aa3b, v131
	v_exp_f32_e32 v133, v133
	v_exp_f32_e32 v144, v144
	v_mul_f32_e32 v124, v128, v124
	v_mul_f32_e32 v125, v129, v125
	v_lshl_add_u64 v[146:147], s[12:13], 0, v[146:147]
	v_add_f32_e32 v128, 1.0, v133
	v_add_f32_e32 v129, 1.0, v144
	v_mul_f32_e32 v133, 0xbfb8aa3b, v116
	v_rcp_f32_e32 v128, v128
	v_rcp_f32_e32 v129, v129
	v_exp_f32_e32 v133, v133
	v_mul_f32_e32 v144, 0xbfb8aa3b, v117
	v_exp_f32_e32 v144, v144
	v_mul_f32_e32 v128, v130, v128
	v_mul_f32_e32 v129, v131, v129
	v_add_f32_e32 v130, 1.0, v133
	v_mul_f32_e32 v133, 0xbfb8aa3b, v118
	v_add_f32_e32 v131, 1.0, v144
	v_exp_f32_e32 v133, v133
	v_mul_f32_e32 v144, 0xbfb8aa3b, v119
	v_exp_f32_e32 v145, v144
	v_rcp_f32_e32 v130, v130
	v_add_f32_e32 v133, 1.0, v133
	v_rcp_f32_e32 v131, v131
	v_rcp_f32_e32 v144, v133
	v_add_f32_e32 v133, 1.0, v145
	v_rcp_f32_e32 v145, v133
	v_mul_f32_e32 v116, v116, v130
	v_mul_f32_e32 v117, v117, v131
	v_mul_f32_e32 v126, v128, v126
	v_mul_f32_e32 v127, v129, v127
	v_mul_f32_e32 v128, v116, v120
	v_mul_f32_e32 v129, v117, v121
	v_mul_f32_e32 v116, v118, v144
	v_mul_f32_e32 v117, v119, v145
	v_lshlrev_b64 v[118:119], 1, v[142:143]
	v_mul_f32_e32 v130, v116, v122
	v_mul_f32_e32 v131, v117, v123
	v_lshl_add_u64 v[116:117], v[146:147], 0, v[118:119]
	v_cvt_pk_bf16_f32 v120, v124, v125
	v_cvt_pk_bf16_f32 v121, v126, v127
	v_cvt_pk_bf16_f32 v122, v128, v129
	v_cvt_pk_bf16_f32 v123, v130, v131
	global_store_dwordx4 v[116:117], v[120:123], off
	s_mov_b32 s2, 0x40000
	s_nop 0
	v_mul_f32_e32 v120, 0xbfb8aa3b, v110
	v_exp_f32_e32 v121, v120
	v_mul_f32_e32 v120, 0xbfb8aa3b, v111
	v_exp_f32_e32 v123, v120
	v_or_b32_e32 v120, 16, v132
	v_add_f32_e32 v121, 1.0, v121
	v_rcp_f32_e32 v122, v121
	v_add_f32_e32 v121, 1.0, v123
	v_rcp_f32_e32 v123, v121
	v_ashrrev_i32_e32 v121, 31, v120
	v_lshlrev_b64 v[120:121], 11, v[120:121]
	v_lshl_add_u64 v[120:121], s[12:13], 0, v[120:121]
	v_mul_f32_e32 v110, v110, v122
	v_mul_f32_e32 v111, v111, v123
	v_mul_f32_e32 v122, 0xbfb8aa3b, v112
	v_mul_f32_e32 v123, 0xbfb8aa3b, v113
	v_exp_f32_e32 v122, v122
	v_exp_f32_e32 v123, v123
	v_mul_f32_e32 v106, v110, v106
	v_mul_f32_e32 v107, v111, v107
	v_add_f32_e32 v110, 1.0, v122
	v_add_f32_e32 v111, 1.0, v123
	v_mul_f32_e32 v122, 0xbfb8aa3b, v98
	v_mul_f32_e32 v123, 0xbfb8aa3b, v99
	v_rcp_f32_e32 v110, v110
	v_rcp_f32_e32 v111, v111
	v_exp_f32_e32 v122, v122
	v_exp_f32_e32 v123, v123
	v_mul_f32_e32 v110, v112, v110
	v_mul_f32_e32 v111, v113, v111
	v_add_f32_e32 v112, 1.0, v122
	v_add_f32_e32 v113, 1.0, v123
	v_mul_f32_e32 v122, 0xbfb8aa3b, v100
	v_mul_f32_e32 v123, 0xbfb8aa3b, v101
	v_exp_f32_e32 v122, v122
	v_exp_f32_e32 v123, v123
	v_rcp_f32_e32 v112, v112
	v_rcp_f32_e32 v113, v113
	v_add_f32_e32 v122, 1.0, v122
	v_add_f32_e32 v123, 1.0, v123
	v_rcp_f32_e32 v122, v122
	v_rcp_f32_e32 v123, v123
	v_mul_f32_e32 v98, v98, v112
	v_mul_f32_e32 v99, v99, v113
	v_mul_f32_e32 v108, v110, v108
	v_mul_f32_e32 v109, v111, v109
	v_mul_f32_e32 v102, v98, v102
	v_mul_f32_e32 v103, v99, v103
	v_mul_f32_e32 v98, v100, v122
	v_mul_f32_e32 v99, v101, v123
	v_lshl_add_u64 v[110:111], v[120:121], 0, v[118:119]
	v_mul_f32_e32 v104, v98, v104
	v_mul_f32_e32 v105, v99, v105
	v_cvt_pk_bf16_f32 v98, v106, v107
	v_cvt_pk_bf16_f32 v99, v108, v109
	v_cvt_pk_bf16_f32 v100, v102, v103
	v_cvt_pk_bf16_f32 v101, v104, v105
	global_store_dwordx4 v[110:111], v[98:101], off
	s_nop 1
	v_mul_f32_e32 v98, 0xbfb8aa3b, v94
	v_exp_f32_e32 v99, v98
	v_mul_f32_e32 v98, 0xbfb8aa3b, v95
	v_exp_f32_e32 v101, v98
	v_or_b32_e32 v98, 32, v132
	v_add_f32_e32 v99, 1.0, v99
	v_rcp_f32_e32 v100, v99
	v_add_f32_e32 v99, 1.0, v101
	v_rcp_f32_e32 v101, v99
	v_ashrrev_i32_e32 v99, 31, v98
	v_lshlrev_b64 v[98:99], 11, v[98:99]
	v_lshl_add_u64 v[98:99], s[12:13], 0, v[98:99]
	v_mul_f32_e32 v94, v94, v100
	v_mul_f32_e32 v95, v95, v101
	v_mul_f32_e32 v100, 0xbfb8aa3b, v96
	v_mul_f32_e32 v101, 0xbfb8aa3b, v97
	v_exp_f32_e32 v100, v100
	v_exp_f32_e32 v101, v101
	v_mul_f32_e32 v90, v94, v90
	v_mul_f32_e32 v91, v95, v91
	v_add_f32_e32 v94, 1.0, v100
	v_add_f32_e32 v95, 1.0, v101
	v_mul_f32_e32 v100, 0xbfb8aa3b, v82
	v_mul_f32_e32 v101, 0xbfb8aa3b, v83
	v_rcp_f32_e32 v94, v94
	v_rcp_f32_e32 v95, v95
	v_exp_f32_e32 v100, v100
	v_exp_f32_e32 v101, v101
	v_mul_f32_e32 v94, v96, v94
	v_mul_f32_e32 v95, v97, v95
	v_add_f32_e32 v96, 1.0, v100
	v_add_f32_e32 v97, 1.0, v101
	v_mul_f32_e32 v100, 0xbfb8aa3b, v84
	v_mul_f32_e32 v101, 0xbfb8aa3b, v85
	v_exp_f32_e32 v100, v100
	v_exp_f32_e32 v101, v101
	v_rcp_f32_e32 v96, v96
	v_rcp_f32_e32 v97, v97
	v_add_f32_e32 v100, 1.0, v100
	v_add_f32_e32 v101, 1.0, v101
	v_rcp_f32_e32 v100, v100
	v_rcp_f32_e32 v101, v101
	v_mul_f32_e32 v82, v82, v96
	v_mul_f32_e32 v83, v83, v97
	v_mul_f32_e32 v92, v94, v92
	v_mul_f32_e32 v93, v95, v93
	v_mul_f32_e32 v86, v82, v86
	v_mul_f32_e32 v87, v83, v87
	v_mul_f32_e32 v82, v84, v100
	v_mul_f32_e32 v83, v85, v101
	v_lshl_add_u64 v[94:95], v[98:99], 0, v[118:119]
	v_mul_f32_e32 v88, v82, v88
	v_mul_f32_e32 v89, v83, v89
	v_cvt_pk_bf16_f32 v82, v90, v91
	v_cvt_pk_bf16_f32 v83, v92, v93
	v_cvt_pk_bf16_f32 v84, v86, v87
	v_cvt_pk_bf16_f32 v85, v88, v89
	global_store_dwordx4 v[94:95], v[82:85], off
	s_nop 1
	v_mul_f32_e32 v82, 0xbfb8aa3b, v78
	v_exp_f32_e32 v83, v82
	v_mul_f32_e32 v82, 0xbfb8aa3b, v79
	v_exp_f32_e32 v85, v82
	v_or_b32_e32 v82, 48, v132
	v_add_f32_e32 v83, 1.0, v83
	v_rcp_f32_e32 v84, v83
	v_add_f32_e32 v83, 1.0, v85
	v_rcp_f32_e32 v85, v83
	v_ashrrev_i32_e32 v83, 31, v82
	v_lshlrev_b64 v[82:83], 11, v[82:83]
	v_lshl_add_u64 v[82:83], s[12:13], 0, v[82:83]
	v_mul_f32_e32 v78, v78, v84
	v_mul_f32_e32 v79, v79, v85
	v_mul_f32_e32 v84, 0xbfb8aa3b, v80
	v_mul_f32_e32 v85, 0xbfb8aa3b, v81
	v_exp_f32_e32 v84, v84
	v_exp_f32_e32 v85, v85
	v_mul_f32_e32 v74, v78, v74
	v_mul_f32_e32 v75, v79, v75
	v_add_f32_e32 v78, 1.0, v84
	v_add_f32_e32 v79, 1.0, v85
	v_mul_f32_e32 v84, 0xbfb8aa3b, v56
	v_mul_f32_e32 v85, 0xbfb8aa3b, v57
	v_rcp_f32_e32 v78, v78
	v_rcp_f32_e32 v79, v79
	v_exp_f32_e32 v84, v84
	v_exp_f32_e32 v85, v85
	v_mul_f32_e32 v78, v80, v78
	v_mul_f32_e32 v79, v81, v79
	v_add_f32_e32 v80, 1.0, v84
	v_add_f32_e32 v81, 1.0, v85
	v_mul_f32_e32 v84, 0xbfb8aa3b, v58
	v_mul_f32_e32 v85, 0xbfb8aa3b, v59
	v_exp_f32_e32 v84, v84
	v_exp_f32_e32 v85, v85
	v_rcp_f32_e32 v80, v80
	v_rcp_f32_e32 v81, v81
	v_add_f32_e32 v84, 1.0, v84
	v_add_f32_e32 v85, 1.0, v85
	v_rcp_f32_e32 v84, v84
	v_rcp_f32_e32 v85, v85
	v_mul_f32_e32 v56, v56, v80
	v_mul_f32_e32 v57, v57, v81
	v_mul_f32_e32 v76, v78, v76
	v_mul_f32_e32 v77, v79, v77
	v_mul_f32_e32 v70, v56, v70
	v_mul_f32_e32 v71, v57, v71
	v_mul_f32_e32 v56, v58, v84
	v_mul_f32_e32 v57, v59, v85
	v_lshl_add_u64 v[78:79], v[82:83], 0, v[118:119]
	v_mul_f32_e32 v72, v56, v72
	v_mul_f32_e32 v73, v57, v73
	v_mul_f32_e32 v57, 0xbfb8aa3b, v66
	v_exp_f32_e32 v58, v57
	v_mul_f32_e32 v57, 0xbfb8aa3b, v67
	v_exp_f32_e32 v59, v57
	v_cvt_pk_bf16_f32 v56, v74, v75
	v_add_f32_e32 v58, 1.0, v58
	v_rcp_f32_e32 v74, v58
	v_add_f32_e32 v58, 1.0, v59
	v_rcp_f32_e32 v75, v58
	v_cvt_pk_bf16_f32 v57, v76, v77
	v_cvt_pk_bf16_f32 v58, v70, v71
	v_cvt_pk_bf16_f32 v59, v72, v73
	global_store_dwordx4 v[78:79], v[56:59], off
	s_nop 1
	v_mul_f32_e32 v56, v66, v74
	v_mul_f32_e32 v57, v67, v75
	v_mul_f32_e32 v66, 0xbfb8aa3b, v50
	v_mul_f32_e32 v56, v56, v60
	v_mul_f32_e32 v57, v57, v61
	v_mul_f32_e32 v60, 0xbfb8aa3b, v48
	v_mul_f32_e32 v61, 0xbfb8aa3b, v49
	v_exp_f32_e32 v60, v60
	v_exp_f32_e32 v61, v61
	v_mul_f32_e32 v67, 0xbfb8aa3b, v51
	v_exp_f32_e32 v66, v66
	v_exp_f32_e32 v67, v67
	v_mul_f32_e32 v58, 0xbfb8aa3b, v68
	v_mul_f32_e32 v59, 0xbfb8aa3b, v69
	v_add_f32_e32 v60, 1.0, v60
	v_add_f32_e32 v61, 1.0, v61
	v_exp_f32_e32 v58, v58
	v_exp_f32_e32 v59, v59
	v_rcp_f32_e32 v60, v60
	v_rcp_f32_e32 v61, v61
	v_add_f32_e32 v66, 1.0, v66
	v_add_f32_e32 v67, 1.0, v67
	v_rcp_f32_e32 v66, v66
	v_rcp_f32_e32 v67, v67
	v_add_f32_e32 v58, 1.0, v58
	v_add_f32_e32 v59, 1.0, v59
	v_mul_f32_e32 v48, v48, v60
	v_mul_f32_e32 v49, v49, v61
	v_rcp_f32_e32 v58, v58
	v_rcp_f32_e32 v59, v59
	v_mul_f32_e32 v52, v48, v52
	v_mul_f32_e32 v53, v49, v53
	v_mul_f32_e32 v48, v50, v66
	v_mul_f32_e32 v49, v51, v67
	v_mul_f32_e32 v51, 0xbfb8aa3b, v44
	v_cvt_pk_bf16_f32 v50, v52, v53
	v_exp_f32_e32 v52, v51
	v_mul_f32_e32 v51, 0xbfb8aa3b, v45
	v_exp_f32_e32 v53, v51
	v_mul_f32_e32 v58, v68, v58
	v_mul_f32_e32 v59, v69, v59
	v_mul_f32_e32 v54, v48, v54
	v_mul_f32_e32 v55, v49, v55
	v_mul_f32_e32 v58, v58, v62
	v_mul_f32_e32 v59, v59, v63
	v_cvt_pk_bf16_f32 v51, v54, v55
	v_add_co_u32_e32 v54, vcc, s2, v116
	v_cvt_pk_bf16_f32 v48, v56, v57
	v_cvt_pk_bf16_f32 v49, v58, v59
	v_add_f32_e32 v52, 1.0, v52
	v_add_f32_e32 v53, 1.0, v53
	v_addc_co_u32_e32 v55, vcc, 0, v117, vcc
	v_rcp_f32_e32 v52, v52
	v_rcp_f32_e32 v53, v53
	global_store_dwordx4 v[54:55], v[48:51], off
	s_mov_b32 s2, 0x48000
	v_mul_f32_e32 v44, v44, v52
	v_mul_f32_e32 v45, v45, v53
	v_mul_f32_e32 v48, 0xbfb8aa3b, v46
	v_mul_f32_e32 v49, 0xbfb8aa3b, v47
	v_exp_f32_e32 v48, v48
	v_exp_f32_e32 v49, v49
	v_mul_f32_e32 v40, v44, v40
	v_mul_f32_e32 v41, v45, v41
	v_add_f32_e32 v44, 1.0, v48
	v_add_f32_e32 v45, 1.0, v49
	v_mul_f32_e32 v48, 0xbfb8aa3b, v32
	v_mul_f32_e32 v49, 0xbfb8aa3b, v33
	v_rcp_f32_e32 v44, v44
	v_rcp_f32_e32 v45, v45
	v_exp_f32_e32 v48, v48
	v_exp_f32_e32 v49, v49
	v_mul_f32_e32 v44, v46, v44
	v_mul_f32_e32 v45, v47, v45
	v_add_f32_e32 v46, 1.0, v48
	v_add_f32_e32 v47, 1.0, v49
	v_mul_f32_e32 v48, 0xbfb8aa3b, v34
	v_mul_f32_e32 v49, 0xbfb8aa3b, v35
	v_exp_f32_e32 v48, v48
	v_exp_f32_e32 v49, v49
	v_rcp_f32_e32 v46, v46
	v_rcp_f32_e32 v47, v47
	v_add_f32_e32 v48, 1.0, v48
	v_add_f32_e32 v49, 1.0, v49
	v_rcp_f32_e32 v48, v48
	v_rcp_f32_e32 v49, v49
	v_mul_f32_e32 v32, v32, v46
	v_mul_f32_e32 v33, v33, v47
	v_mul_f32_e32 v42, v44, v42
	v_mul_f32_e32 v43, v45, v43
	v_mul_f32_e32 v36, v32, v36
	v_mul_f32_e32 v37, v33, v37
	v_mul_f32_e32 v32, v34, v48
	v_mul_f32_e32 v33, v35, v49
	v_mul_f32_e32 v35, 0xbfb8aa3b, v28
	v_cvt_pk_bf16_f32 v34, v36, v37
	v_exp_f32_e32 v36, v35
	v_mul_f32_e32 v35, 0xbfb8aa3b, v29
	v_exp_f32_e32 v37, v35
	v_mul_f32_e32 v38, v32, v38
	v_mul_f32_e32 v39, v33, v39
	v_cvt_pk_bf16_f32 v32, v40, v41
	v_cvt_pk_bf16_f32 v35, v38, v39
	v_add_co_u32_e32 v38, vcc, s2, v116
	v_cvt_pk_bf16_f32 v33, v42, v43
	v_add_f32_e32 v36, 1.0, v36
	v_add_f32_e32 v37, 1.0, v37
	v_addc_co_u32_e32 v39, vcc, 0, v117, vcc
	v_rcp_f32_e32 v36, v36
	v_rcp_f32_e32 v37, v37
	global_store_dwordx4 v[38:39], v[32:35], off
	s_mov_b32 s2, 0x50000
	v_mul_f32_e32 v28, v28, v36
	v_mul_f32_e32 v29, v29, v37
	v_mul_f32_e32 v32, 0xbfb8aa3b, v30
	v_mul_f32_e32 v33, 0xbfb8aa3b, v31
	v_exp_f32_e32 v32, v32
	v_exp_f32_e32 v33, v33
	v_mul_f32_e32 v24, v28, v24
	v_mul_f32_e32 v25, v29, v25
	v_add_f32_e32 v28, 1.0, v32
	v_add_f32_e32 v29, 1.0, v33
	v_mul_f32_e32 v32, 0xbfb8aa3b, v16
	v_mul_f32_e32 v33, 0xbfb8aa3b, v17
	v_rcp_f32_e32 v28, v28
	v_rcp_f32_e32 v29, v29
	v_exp_f32_e32 v32, v32
	v_exp_f32_e32 v33, v33
	v_mul_f32_e32 v28, v30, v28
	v_mul_f32_e32 v29, v31, v29
	v_add_f32_e32 v30, 1.0, v32
	v_add_f32_e32 v31, 1.0, v33
	v_mul_f32_e32 v32, 0xbfb8aa3b, v18
	v_mul_f32_e32 v33, 0xbfb8aa3b, v19
	v_exp_f32_e32 v32, v32
	v_exp_f32_e32 v33, v33
	v_rcp_f32_e32 v30, v30
	v_rcp_f32_e32 v31, v31
	v_add_f32_e32 v32, 1.0, v32
	v_add_f32_e32 v33, 1.0, v33
	v_rcp_f32_e32 v32, v32
	v_rcp_f32_e32 v33, v33
	v_mul_f32_e32 v16, v16, v30
	v_mul_f32_e32 v17, v17, v31
	v_mul_f32_e32 v26, v28, v26
	v_mul_f32_e32 v27, v29, v27
	v_mul_f32_e32 v20, v16, v20
	v_mul_f32_e32 v21, v17, v21
	v_mul_f32_e32 v16, v18, v32
	v_mul_f32_e32 v17, v19, v33
	v_mul_f32_e32 v19, 0xbfb8aa3b, v12
	v_cvt_pk_bf16_f32 v18, v20, v21
	v_exp_f32_e32 v20, v19
	v_mul_f32_e32 v19, 0xbfb8aa3b, v13
	v_exp_f32_e32 v21, v19
	v_mul_f32_e32 v22, v16, v22
	v_mul_f32_e32 v23, v17, v23
	v_cvt_pk_bf16_f32 v16, v24, v25
	v_cvt_pk_bf16_f32 v19, v22, v23
	v_add_co_u32_e32 v22, vcc, s2, v116
	v_cvt_pk_bf16_f32 v17, v26, v27
	v_add_f32_e32 v20, 1.0, v20
	v_add_f32_e32 v21, 1.0, v21
	v_addc_co_u32_e32 v23, vcc, 0, v117, vcc
	v_rcp_f32_e32 v20, v20
	v_rcp_f32_e32 v21, v21
	global_store_dwordx4 v[22:23], v[16:19], off
	v_mul_f32_e32 v12, v12, v20
	v_mul_f32_e32 v13, v13, v21
	s_nop 0
	v_mul_f32_e32 v16, 0xbfb8aa3b, v14
	v_mul_f32_e32 v17, 0xbfb8aa3b, v15
	v_exp_f32_e32 v16, v16
	v_exp_f32_e32 v17, v17
	v_mul_f32_e32 v8, v12, v8
	v_mul_f32_e32 v9, v13, v9
	v_add_f32_e32 v12, 1.0, v16
	v_add_f32_e32 v13, 1.0, v17
	v_mul_f32_e32 v16, 0xbfb8aa3b, v0
	v_mul_f32_e32 v17, 0xbfb8aa3b, v1
	v_rcp_f32_e32 v12, v12
	v_rcp_f32_e32 v13, v13
	v_exp_f32_e32 v16, v16
	v_exp_f32_e32 v17, v17
	v_mul_f32_e32 v12, v14, v12
	v_mul_f32_e32 v13, v15, v13
	v_add_f32_e32 v14, 1.0, v16
	v_add_f32_e32 v15, 1.0, v17
	v_mul_f32_e32 v16, 0xbfb8aa3b, v2
	v_mul_f32_e32 v17, 0xbfb8aa3b, v3
	v_exp_f32_e32 v16, v16
	v_exp_f32_e32 v17, v17
	v_rcp_f32_e32 v14, v14
	v_rcp_f32_e32 v15, v15
	v_add_f32_e32 v16, 1.0, v16
	v_add_f32_e32 v17, 1.0, v17
	v_rcp_f32_e32 v16, v16
	v_rcp_f32_e32 v17, v17
	v_mul_f32_e32 v0, v0, v14
	v_mul_f32_e32 v1, v1, v15
	v_mul_f32_e32 v10, v12, v10
	v_mul_f32_e32 v11, v13, v11
	v_mul_f32_e32 v4, v0, v4
	v_mul_f32_e32 v5, v1, v5
	v_mul_f32_e32 v0, v2, v16
	v_mul_f32_e32 v1, v3, v17
	v_cvt_pk_bf16_f32 v2, v4, v5
	v_add_co_u32_e32 v4, vcc, 0x58000, v116
	v_mul_f32_e32 v6, v0, v6
	v_mul_f32_e32 v7, v1, v7
	s_nop 0
	v_addc_co_u32_e32 v5, vcc, 0, v117, vcc
	v_cvt_pk_bf16_f32 v0, v8, v9
	v_cvt_pk_bf16_f32 v1, v10, v11
	v_cvt_pk_bf16_f32 v3, v6, v7
	s_and_b64 vcc, exec, s[0:1]
	s_mov_b64 s[0:1], -1
	global_store_dwordx4 v[4:5], v[0:3], off
	s_cbranch_vccnz .LBB0_1417
	s_andn2_b64 vcc, exec, s[10:11]
	s_cbranch_vccnz .LBB0_1416
	s_barrier
	s_branch .LBB0_1416

.LBB0_1509:
	s_lshl_b32 s4, s20, 8
	v_mbcnt_lo_u32_b32 v132, -1, 0
	v_mbcnt_hi_u32_b32 v132, -1, v132
	s_add_i32 s4, s4, s21
	v_and_or_b32 v136, v132, 15, s4
	s_lshl_b32 s4, s60, 8
	v_ashrrev_i32_e32 v132, 1, v132
	s_or_b32 s4, s4, s50
	v_and_b32_e32 v132, -8, v132
	v_add_u32_e32 v132, s4, v132
	v_ashrrev_i32_e32 v137, 31, v136
	v_ashrrev_i32_e32 v133, 31, v132
	v_lshlrev_b64 v[134:135], 11, v[136:137]
	v_lshl_add_u64 v[134:135], s[8:9], 0, v[134:135]
	v_lshlrev_b64 v[138:139], 1, v[132:133]
	v_lshl_add_u64 v[132:133], v[134:135], 0, v[138:139]
	v_lshl_add_u64 v[134:135], v[136:137], 2, s[2:3]
	s_mov_b64 s[4:5], 0x40000
	s_waitcnt vmcnt(16) lgkmcnt(0)
	v_mov_b32_e32 v146, v244
	v_mov_b32_e32 v148, v245
	v_mov_b32_e32 v150, v246
	v_mov_b32_e32 v152, v247
	v_mov_b32_e32 v154, v248
	v_mov_b32_e32 v156, v249
	v_mov_b32_e32 v158, v250
	v_mov_b32_e32 v160, v251
	v_mul_f32_e32 v118, v118, v146
	v_mul_f32_e32 v119, v119, v146
	v_mul_f32_e32 v116, v116, v146
	v_mul_f32_e32 v117, v117, v146
	v_mul_f32_e32 v122, v122, v146
	v_mul_f32_e32 v123, v123, v146
	v_mul_f32_e32 v120, v120, v146
	v_mul_f32_e32 v121, v121, v146
	v_cvt_pk_bf16_f32 v116, v116, v117
	v_cvt_pk_bf16_f32 v117, v118, v119
	v_cvt_pk_bf16_f32 v118, v120, v121
	v_cvt_pk_bf16_f32 v119, v122, v123
	global_store_dwordx4 v[132:133], v[116:119], off
	v_mul_f32_e32 v120, v130, v146
	v_mul_f32_e32 v121, v131, v146
	v_mul_f32_e32 v122, v128, v146
	v_mul_f32_e32 v123, v129, v146
	v_mul_f32_e32 v118, v126, v146
	v_mul_f32_e32 v119, v127, v146
	v_mul_f32_e32 v116, v124, v146
	v_mul_f32_e32 v117, v125, v146
	s_nop 0
	v_cvt_pk_bf16_f32 v116, v116, v117
	v_cvt_pk_bf16_f32 v117, v118, v119
	v_cvt_pk_bf16_f32 v118, v122, v123
	v_cvt_pk_bf16_f32 v119, v120, v121
	global_store_dwordx4 v[132:133], v[116:119], off offset:256
	s_nop 1
	v_or_b32_e32 v116, 16, v136
	v_ashrrev_i32_e32 v117, 31, v116
	v_lshlrev_b64 v[118:119], 11, v[116:117]
	v_lshl_add_u64 v[116:117], v[116:117], 2, s[2:3]
	s_nop 0
	v_lshl_add_u64 v[118:119], s[8:9], 0, v[118:119]
	v_lshl_add_u64 v[118:119], v[118:119], 0, v[138:139]
	s_nop 0
	v_mul_f32_e32 v100, v100, v148
	v_mul_f32_e32 v101, v101, v148
	v_mul_f32_e32 v98, v98, v148
	v_mul_f32_e32 v99, v99, v148
	v_mul_f32_e32 v104, v104, v148
	v_mul_f32_e32 v105, v105, v148
	v_mul_f32_e32 v102, v102, v148
	v_mul_f32_e32 v103, v103, v148
	v_cvt_pk_bf16_f32 v98, v98, v99
	v_cvt_pk_bf16_f32 v99, v100, v101
	v_cvt_pk_bf16_f32 v100, v102, v103
	v_cvt_pk_bf16_f32 v101, v104, v105
	global_store_dwordx4 v[118:119], v[98:101], off
	v_mul_f32_e32 v102, v112, v148
	v_mul_f32_e32 v103, v113, v148
	v_mul_f32_e32 v104, v110, v148
	v_mul_f32_e32 v105, v111, v148
	v_mul_f32_e32 v100, v108, v148
	v_mul_f32_e32 v101, v109, v148
	v_mul_f32_e32 v98, v106, v148
	v_mul_f32_e32 v99, v107, v148
	s_nop 0
	v_cvt_pk_bf16_f32 v98, v98, v99
	v_cvt_pk_bf16_f32 v99, v100, v101
	v_cvt_pk_bf16_f32 v100, v104, v105
	v_cvt_pk_bf16_f32 v101, v102, v103
	global_store_dwordx4 v[118:119], v[98:101], off offset:256
	s_nop 1
	v_or_b32_e32 v98, 32, v136
	v_ashrrev_i32_e32 v99, 31, v98
	v_lshlrev_b64 v[100:101], 11, v[98:99]
	v_lshl_add_u64 v[98:99], v[98:99], 2, s[2:3]
	s_nop 0
	v_lshl_add_u64 v[100:101], s[8:9], 0, v[100:101]
	v_lshl_add_u64 v[100:101], v[100:101], 0, v[138:139]
	s_nop 0
	v_mul_f32_e32 v84, v84, v150
	v_mul_f32_e32 v85, v85, v150
	v_mul_f32_e32 v82, v82, v150
	v_mul_f32_e32 v83, v83, v150
	v_mul_f32_e32 v88, v88, v150
	v_mul_f32_e32 v89, v89, v150
	v_mul_f32_e32 v86, v86, v150
	v_mul_f32_e32 v87, v87, v150
	v_cvt_pk_bf16_f32 v82, v82, v83
	v_cvt_pk_bf16_f32 v83, v84, v85
	v_cvt_pk_bf16_f32 v84, v86, v87
	v_cvt_pk_bf16_f32 v85, v88, v89
	global_store_dwordx4 v[100:101], v[82:85], off
	v_mul_f32_e32 v86, v96, v150
	v_mul_f32_e32 v87, v97, v150
	v_mul_f32_e32 v88, v94, v150
	v_mul_f32_e32 v89, v95, v150
	v_mul_f32_e32 v84, v92, v150
	v_mul_f32_e32 v85, v93, v150
	v_mul_f32_e32 v82, v90, v150
	v_mul_f32_e32 v83, v91, v150
	s_nop 0
	v_cvt_pk_bf16_f32 v82, v82, v83
	v_cvt_pk_bf16_f32 v83, v84, v85
	v_cvt_pk_bf16_f32 v84, v88, v89
	v_cvt_pk_bf16_f32 v85, v86, v87
	global_store_dwordx4 v[100:101], v[82:85], off offset:256
	s_nop 1
	v_or_b32_e32 v82, 48, v136
	v_ashrrev_i32_e32 v83, 31, v82
	v_lshlrev_b64 v[84:85], 11, v[82:83]
	v_lshl_add_u64 v[82:83], v[82:83], 2, s[2:3]
	s_nop 0
	v_lshl_add_u64 v[84:85], s[8:9], 0, v[84:85]
	v_lshl_add_u64 v[84:85], v[84:85], 0, v[138:139]
	s_nop 0
	v_mul_f32_e32 v80, v80, v152
	v_mul_f32_e32 v81, v81, v152
	v_mul_f32_e32 v78, v78, v152
	v_mul_f32_e32 v79, v79, v152
	v_mul_f32_e32 v86, v76, v152
	v_mul_f32_e32 v87, v77, v152
	v_mul_f32_e32 v76, v74, v152
	v_mul_f32_e32 v77, v75, v152
	v_cvt_pk_bf16_f32 v74, v78, v79
	v_cvt_pk_bf16_f32 v75, v80, v81
	v_cvt_pk_bf16_f32 v76, v76, v77
	v_cvt_pk_bf16_f32 v77, v86, v87
	global_store_dwordx4 v[84:85], v[74:77], off
	v_mul_f32_e32 v62, v62, v152
	v_mul_f32_e32 v63, v63, v152
	v_mul_f32_e32 v60, v60, v152
	v_mul_f32_e32 v61, v61, v152
	v_mul_f32_e32 v74, v58, v152
	v_mul_f32_e32 v75, v59, v152
	v_mul_f32_e32 v58, v56, v152
	v_mul_f32_e32 v59, v57, v152
	v_cvt_pk_bf16_f32 v56, v60, v61
	v_cvt_pk_bf16_f32 v57, v62, v63
	v_cvt_pk_bf16_f32 v58, v58, v59
	v_cvt_pk_bf16_f32 v59, v74, v75
	global_store_dwordx4 v[84:85], v[56:59], off offset:256
	s_nop 0
	v_lshl_add_u64 v[60:61], v[132:133], 0, s[4:5]
	s_mov_b32 s4, 0x40000
	s_nop 0
	v_mul_f32_e32 v58, v68, v154
	v_mul_f32_e32 v59, v69, v154
	v_mul_f32_e32 v56, v66, v154
	v_mul_f32_e32 v57, v67, v154
	v_mul_f32_e32 v66, v72, v154
	v_mul_f32_e32 v67, v73, v154
	v_mul_f32_e32 v68, v70, v154
	v_mul_f32_e32 v69, v71, v154
	v_cvt_pk_bf16_f32 v56, v56, v57
	v_cvt_pk_bf16_f32 v57, v58, v59
	v_cvt_pk_bf16_f32 v59, v66, v67
	v_add_co_u32_e32 v66, vcc, s4, v132
	v_cvt_pk_bf16_f32 v58, v68, v69
	s_nop 0
	v_addc_co_u32_e32 v67, vcc, 0, v133, vcc
	global_store_dwordx4 v[66:67], v[56:59], off
	v_mul_f32_e32 v54, v54, v154
	v_mul_f32_e32 v55, v55, v154
	v_mul_f32_e32 v52, v52, v154
	v_mul_f32_e32 v53, v53, v154
	v_mul_f32_e32 v56, v50, v154
	v_mul_f32_e32 v57, v51, v154
	v_mul_f32_e32 v50, v48, v154
	v_mul_f32_e32 v51, v49, v154
	v_cvt_pk_bf16_f32 v48, v52, v53
	v_cvt_pk_bf16_f32 v49, v54, v55
	v_cvt_pk_bf16_f32 v50, v50, v51
	v_cvt_pk_bf16_f32 v51, v56, v57
	global_store_dwordx4 v[60:61], v[48:51], off offset:256
	s_nop 0
	s_mov_b64 s[4:5], 0x48000
	v_lshl_add_u64 v[48:49], v[132:133], 0, s[4:5]
	s_mov_b32 s4, 0x48000
	s_nop 0
	v_mul_f32_e32 v42, v42, v156
	v_mul_f32_e32 v43, v43, v156
	v_mul_f32_e32 v40, v40, v156
	v_mul_f32_e32 v41, v41, v156
	v_mul_f32_e32 v44, v44, v156
	v_mul_f32_e32 v45, v45, v156
	v_mul_f32_e32 v46, v46, v156
	v_mul_f32_e32 v47, v47, v156
	v_cvt_pk_bf16_f32 v40, v40, v41
	v_cvt_pk_bf16_f32 v41, v42, v43
	v_cvt_pk_bf16_f32 v42, v44, v45
	v_add_co_u32_e32 v44, vcc, s4, v132
	v_cvt_pk_bf16_f32 v43, v46, v47
	s_nop 0
	v_addc_co_u32_e32 v45, vcc, 0, v133, vcc
	global_store_dwordx4 v[44:45], v[40:43], off
	v_mul_f32_e32 v38, v38, v156
	v_mul_f32_e32 v39, v39, v156
	v_mul_f32_e32 v36, v36, v156
	v_mul_f32_e32 v37, v37, v156
	v_mul_f32_e32 v40, v34, v156
	v_mul_f32_e32 v41, v35, v156
	v_mul_f32_e32 v34, v32, v156
	v_mul_f32_e32 v35, v33, v156
	v_cvt_pk_bf16_f32 v32, v36, v37
	v_cvt_pk_bf16_f32 v33, v38, v39
	v_cvt_pk_bf16_f32 v34, v34, v35
	v_cvt_pk_bf16_f32 v35, v40, v41
	global_store_dwordx4 v[48:49], v[32:35], off offset:256
	s_nop 0
	s_mov_b64 s[4:5], 0x50000
	v_lshl_add_u64 v[32:33], v[132:133], 0, s[4:5]
	s_mov_b32 s4, 0x50000
	s_nop 0
	v_mul_f32_e32 v26, v26, v158
	v_mul_f32_e32 v27, v27, v158
	v_mul_f32_e32 v24, v24, v158
	v_mul_f32_e32 v25, v25, v158
	v_mul_f32_e32 v28, v28, v158
	v_mul_f32_e32 v29, v29, v158
	v_mul_f32_e32 v30, v30, v158
	v_mul_f32_e32 v31, v31, v158
	v_cvt_pk_bf16_f32 v24, v24, v25
	v_cvt_pk_bf16_f32 v25, v26, v27
	v_cvt_pk_bf16_f32 v26, v28, v29
	v_add_co_u32_e32 v28, vcc, s4, v132
	v_cvt_pk_bf16_f32 v27, v30, v31
	s_nop 0
	v_addc_co_u32_e32 v29, vcc, 0, v133, vcc
	global_store_dwordx4 v[28:29], v[24:27], off
	v_mul_f32_e32 v22, v22, v158
	v_mul_f32_e32 v23, v23, v158
	v_mul_f32_e32 v20, v20, v158
	v_mul_f32_e32 v21, v21, v158
	v_mul_f32_e32 v24, v18, v158
	v_mul_f32_e32 v25, v19, v158
	v_mul_f32_e32 v18, v16, v158
	v_mul_f32_e32 v19, v17, v158
	v_cvt_pk_bf16_f32 v16, v20, v21
	v_cvt_pk_bf16_f32 v17, v22, v23
	v_cvt_pk_bf16_f32 v18, v18, v19
	v_cvt_pk_bf16_f32 v19, v24, v25
	global_store_dwordx4 v[32:33], v[16:19], off offset:256
	s_nop 0
	s_mov_b64 s[4:5], 0x58000
	v_lshl_add_u64 v[18:19], v[132:133], 0, s[4:5]
	s_mov_b32 s4, 0x58000
	s_nop 0
	v_mul_f32_e32 v2, v2, v160
	v_mul_f32_e32 v3, v3, v160
	v_mul_f32_e32 v0, v0, v160
	v_mul_f32_e32 v1, v1, v160
	v_mul_f32_e32 v4, v4, v160
	v_mul_f32_e32 v5, v5, v160
	v_mul_f32_e32 v6, v6, v160
	v_mul_f32_e32 v7, v7, v160
	v_cvt_pk_bf16_f32 v0, v0, v1
	v_cvt_pk_bf16_f32 v1, v2, v3
	v_cvt_pk_bf16_f32 v2, v4, v5
	v_add_co_u32_e32 v4, vcc, s4, v132
	v_cvt_pk_bf16_f32 v3, v6, v7
	s_nop 0
	v_addc_co_u32_e32 v5, vcc, 0, v133, vcc
	global_store_dwordx4 v[4:5], v[0:3], off
	v_mul_f32_e32 v4, v14, v160
	v_mul_f32_e32 v5, v15, v160
	v_mul_f32_e32 v6, v12, v160
	v_mul_f32_e32 v7, v13, v160
	v_mul_f32_e32 v2, v10, v160
	v_mul_f32_e32 v3, v11, v160
	v_mul_f32_e32 v0, v8, v160
	v_mul_f32_e32 v1, v9, v160
	s_mov_b64 s[4:5], -1
	v_cvt_pk_bf16_f32 v0, v0, v1
	v_cvt_pk_bf16_f32 v1, v2, v3
	v_cvt_pk_bf16_f32 v2, v6, v7
	v_cvt_pk_bf16_f32 v3, v4, v5
	s_and_b64 vcc, exec, s[0:1]
	global_store_dwordx4 v[18:19], v[0:3], off offset:256
	s_cbranch_vccnz .LBB0_1500
	s_andn2_b64 vcc, exec, s[6:7]
	s_cbranch_vccnz .LBB0_1499
	s_barrier
	s_branch .LBB0_1499
